# v14 + nt on conv/transpose/route streaming loads
# baseline (speedup 1.0000x reference)
; #define LAS __attribute__((address_space(3)))
; __device__ __forceinline__ int tid_fresh() { int t = threadIdx.x; asm volatile("" : "+v"(t)); return t; }
; __device__ __forceinline__ void hy_conv_phase(LAS unsigned char* lds, int bid, int G, const bf16_t* u, const float* cw, const float* cb, bf16_t* x0c, bf16_t* vgT) {
;     LAS float* sm = (LAS float*)lds;
;     const int tid = tid_fresh();
;     ...
;     u32x4 pv[4];
;     if (bid < 4096) HC_LOAD(bid, pv);
.LBB0_304:
	s_or_b64 exec, exec, s[0:1]
	v_readlane_b32 s2, v254, 19
	s_cmpk_lt_i32 s2, 0x1000
	v_readlane_b32 s0, v254, 0
	s_cselect_b64 s[18:19], -1, 0
	v_readlane_b32 s1, v254, 1
	v_mov_b32_e32 v18, v0
	s_and_b64 vcc, exec, s[18:19]
	s_waitcnt lgkmcnt(0)
	s_barrier
	v_readlane_b32 s3, v254, 20
	s_cbranch_vccz .LBB0_322
	s_load_dwordx2 s[2:3], s[0:1], 0x118
	s_load_dwordx4 s[8:11], s[0:1], 0x38
	v_min_i32_e32 v6, 0x62f, v18
	s_mov_b32 s17, 0x3e0f83e1
	v_mul_hi_i32 v1, v6, s17
	s_waitcnt lgkmcnt(0)
	s_add_u32 s14, s2, 0x49a50000
	s_addc_u32 s15, s3, 0
	s_add_u32 s20, s2, 0x4c250000
	v_readlane_b32 s28, v254, 19
	v_lshrrev_b32_e32 v2, 31, v1
	v_ashrrev_i32_e32 v1, 7, v1
	s_addc_u32 s21, s3, 0
	s_lshl_b32 s40, s28, 1
	v_add_u32_e32 v4, v1, v2
	s_movk_i32 s26, 0xfdf0
	s_and_b32 s0, s40, 0xffffffc0
	v_mad_i32_i24 v1, v4, s26, v6
	v_readlane_b32 s29, v254, 20
	s_add_i32 s0, s0, -1
	v_ashrrev_i32_e32 v1, 3, v1
	s_lshl_b32 s29, s28, 6
	v_add_u32_e32 v2, s0, v1
	v_mov_b32_e32 v45, 0x1fff
	s_add_u32 s24, s2, 0x43650000
	v_med3_i32 v2, v2, 0, v45
	v_lshlrev_b32_e32 v4, 11, v4
	s_addc_u32 s25, s3, 0
	v_mul_u32_u24_e32 v42, 0x1800, v2
	v_mov_b32_e32 v43, 0
	v_ashrrev_i32_e32 v5, 31, v4
	v_lshl_add_u64 v[2:3], v[42:43], 1, s[24:25]
	v_lshlrev_b64 v[20:21], 1, v[4:5]
	s_lshl_b32 s1, s28, 7
	v_lshlrev_b32_e32 v4, 3, v6
	s_mov_b32 s23, 0
	v_lshl_add_u64 v[2:3], v[2:3], 0, v[20:21]
	s_and_b32 s22, s1, 0xf80
	v_and_b32_e32 v22, 56, v4
	v_lshl_add_u64 v[2:3], v[2:3], 0, s[22:23]
	v_lshlrev_b32_e32 v42, 1, v22
	v_min_i32_e32 v6, 0x42f, v18
	v_lshl_add_u64 v[10:11], v[2:3], 0, v[42:43]
	v_add_u32_e32 v2, 0x200, v6
	v_mul_hi_i32 v3, v2, s17
	v_lshrrev_b32_e32 v4, 31, v3
	v_ashrrev_i32_e32 v3, 7, v3
	v_add_u32_e32 v4, v3, v4
	v_mad_i32_i24 v2, v4, s26, v2
	v_ashrrev_i32_e32 v2, 3, v2
	v_add_u32_e32 v2, s0, v2
	v_med3_i32 v2, v2, 0, v45
	v_mul_u32_u24_e32 v42, 0x1800, v2
	v_lshlrev_b32_e32 v4, 11, v4
	v_lshl_add_u64 v[2:3], v[42:43], 1, s[24:25]
	v_ashrrev_i32_e32 v5, 31, v4
	v_lshl_add_u64 v[2:3], v[4:5], 1, v[2:3]
	v_lshlrev_b32_e32 v4, 4, v6
	v_lshl_add_u64 v[2:3], v[2:3], 0, s[22:23]
	v_and_b32_e32 v42, 0x70, v4
	v_min_i32_e32 v14, 0x22f, v18
	v_lshl_add_u64 v[12:13], v[2:3], 0, v[42:43]
	global_load_dwordx4 v[2:5], v[10:11], off nt
	global_load_dwordx4 v[6:9], v[12:13], off nt
	v_add_u32_e32 v10, 0x400, v14
	v_mul_hi_i32 v11, v10, s17
	v_lshrrev_b32_e32 v12, 31, v11
	v_ashrrev_i32_e32 v11, 7, v11
	v_add_u32_e32 v12, v11, v12
	v_mad_i32_i24 v10, v12, s26, v10
	v_ashrrev_i32_e32 v10, 3, v10
	v_add_u32_e32 v10, s0, v10
	v_med3_i32 v10, v10, 0, v45
	v_mul_u32_u24_e32 v42, 0x1800, v10
	v_lshlrev_b32_e32 v12, 11, v12
	v_lshl_add_u64 v[10:11], v[42:43], 1, s[24:25]
	v_ashrrev_i32_e32 v13, 31, v12
	v_lshl_add_u64 v[10:11], v[12:13], 1, v[10:11]
	v_lshlrev_b32_e32 v12, 4, v14
	v_lshl_add_u64 v[10:11], v[10:11], 0, s[22:23]
	v_and_b32_e32 v42, 0x70, v12
	v_min_i32_e32 v14, 47, v18
	v_lshl_add_u64 v[24:25], v[10:11], 0, v[42:43]
	v_add_u32_e32 v10, 0x600, v14
	v_mul_hi_i32 v11, v10, s17
	v_lshrrev_b32_e32 v12, 31, v11
	v_ashrrev_i32_e32 v11, 7, v11
	v_add_u32_e32 v12, v11, v12
	v_mad_i32_i24 v10, v12, s26, v10
	v_ashrrev_i32_e32 v10, 3, v10
	v_add_u32_e32 v10, s0, v10
	v_med3_i32 v10, v10, 0, v45
	v_mul_u32_u24_e32 v42, 0x1800, v10
	v_lshlrev_b32_e32 v12, 11, v12
	v_lshl_add_u64 v[10:11], v[42:43], 1, s[24:25]
	v_ashrrev_i32_e32 v13, 31, v12
	v_lshl_add_u64 v[10:11], v[12:13], 1, v[10:11]
	v_lshlrev_b32_e32 v12, 4, v14
	v_lshl_add_u64 v[10:11], v[10:11], 0, s[22:23]
	v_and_b32_e32 v42, 0x70, v12
	v_lshl_add_u64 v[26:27], v[10:11], 0, v[42:43]
	global_load_dwordx4 v[10:13], v[24:25], off nt
	global_load_dwordx4 v[14:17], v[26:27], off nt
	v_lshlrev_b32_e32 v19, 3, v18
	v_and_b32_e32 v44, 56, v19
	v_ashrrev_i32_e32 v96, 3, v18
	v_lshl_add_u32 v24, v44, 2, 0
; #define LAS __attribute__((address_space(3)))
; __device__ __forceinline__ float bf_lo(unsigned w) { return __uint_as_float(w << 16); }
; __device__ __forceinline__ float bf_hi(unsigned w) { return __uint_as_float(w & 0xffff0000u); }
; __device__ __forceinline__ void hy_conv_phase(LAS unsigned char* lds, int bid, int G, const bf16_t* u, const float* cw, const float* cb, bf16_t* x0c, bf16_t* vgT) {
;     ...
;     float wa[8], wb[8], wc_[8], wd[8]; float p0 = 0.f, p1 = 0.f, p2 = 0.f, pb = 0.f, q0 = 0.f, q1 = 0.f, q2 = 0.f, qb = 0.f; int cwc0 = -1;
;     for (int tile = bid; tile < 4096; tile += G) {
;         const int t0 = (tile >> 5) * 64, c0 = (tile & 31) * 64;
;         if (c0 != cwc0) { cwc0 = c0;
; #pragma unroll
;             for (int q = 0; q < 8; ++q) { const int cc = c0 + (tid & 7) * 8 + q; wa[q] = cw[cc]; wb[q] = cw[6144 + cc]; wc_[q] = cw[12288 + cc]; wd[q] = cb[cc]; }
;             const int c1 = 2048 + c0 + (tid >> 3), c2 = 4096 + c0 + (tid >> 3);
;             p0 = cw[c1]; p1 = cw[6144 + c1]; p2 = cw[12288 + c1]; pb = cb[c1]; q0 = cw[c2]; q1 = cw[6144 + c2]; q2 = cw[12288 + c2]; qb = cb[c2]; }
;         __syncthreads();
; #pragma unroll
;         for (int it = 0; it < 4; ++it) { const int id = tid + NTHR * it;
;             if (id < 3 * 66 * 8) { const int g = id / 528, r = id - g * 528, row = r >> 3, ch = r & 7; const u32x4 v = pv[it];
;                 const int tr = t0 - 1 + row; const float mk = (tr >= 0 && tr < T) ? 1.f : 0.f;
;                 LAS float* dp = sm + (g * 66 + row) * 65 + ch * 8;
;                 dp[0] = bf_lo(v.x) * mk; dp[1] = bf_hi(v.x) * mk; dp[2] = bf_lo(v.y) * mk; dp[3] = bf_hi(v.y) * mk; dp[4] = bf_lo(v.z) * mk; dp[5] = bf_hi(v.z) * mk; dp[6] = bf_lo(v.w) * mk; dp[7] = bf_hi(v.w) * mk; } }
;         if (tile + G < 4096) HC_LOAD(tile + G, pv);
	v_lshlrev_b32_e32 v19, 8, v44
	v_lshlrev_b32_e32 v23, 2, v96
	v_add3_u32 v99, v24, v19, v23
	v_mul_hi_i32 v19, v18, s17
	v_lshrrev_b32_e32 v25, 31, v19
	v_ashrrev_i32_e32 v19, 7, v19
	v_add_u32_e32 v19, v19, v25
	v_mad_i32_i24 v25, v19, s26, v18
	v_ashrrev_i32_e32 v100, 3, v25
	s_movk_i32 s22, 0x42
	v_mad_i32_i24 v19, v19, s22, v100
	s_movk_i32 s27, 0x104
	v_mul_lo_u32 v25, v19, s27
	v_add_u32_e32 v19, 0x200, v18
	v_mul_hi_i32 v26, v19, s17
	v_lshrrev_b32_e32 v27, 31, v26
	v_ashrrev_i32_e32 v26, 7, v26
	v_add_u32_e32 v26, v26, v27
	v_mad_i32_i24 v27, v26, s26, v19
	v_ashrrev_i32_e32 v101, 3, v27
	v_mad_i32_i24 v26, v26, s22, v101
	v_mul_lo_u32 v28, v26, s27
	v_add_u32_e32 v26, 0x400, v18
	v_mul_hi_i32 v27, v26, s17
	v_lshrrev_b32_e32 v29, 31, v27
	v_ashrrev_i32_e32 v27, 7, v27
	v_add_u32_e32 v27, v27, v29
	v_mad_i32_i24 v29, v27, s26, v26
	v_ashrrev_i32_e32 v102, 3, v29
	v_mad_i32_i24 v27, v27, s22, v102
	s_movk_i32 s0, 0x630
	s_movk_i32 s2, 0x430
	s_movk_i32 s4, 0x230
	v_mul_lo_u32 v29, v27, s27
	v_add_u32_e32 v27, 0x600, v18
	v_cmp_gt_i32_e64 s[0:1], s0, v18
	v_cmp_gt_i32_e64 s[2:3], s2, v18
	v_cmp_gt_i32_e64 s[4:5], s4, v18
	v_cmp_gt_i32_e64 s[6:7], 48, v18
	v_mul_hi_i32 v18, v27, s17
	v_lshrrev_b32_e32 v30, 31, v18
	v_ashrrev_i32_e32 v18, 7, v18
	v_add_u32_e32 v18, v18, v30
	v_mad_i32_i24 v30, v18, s26, v27
	v_ashrrev_i32_e32 v103, 3, v30
	v_mad_i32_i24 v18, v18, s22, v103
	v_lshl_add_u64 v[46:47], s[24:25], 0, v[20:21]
	v_min_i32_e32 v20, 0x62f, v19
	v_mul_lo_u32 v30, v18, s27
	v_mul_hi_i32 v18, v20, s17
	v_lshrrev_b32_e32 v19, 31, v18
	v_ashrrev_i32_e32 v18, 7, v18
	v_add_u32_e32 v18, v18, v19
	v_mad_i32_i24 v19, v18, s26, v20
	v_lshlrev_b32_e32 v18, 11, v18
	v_ashrrev_i32_e32 v104, 3, v19
	v_ashrrev_i32_e32 v19, 31, v18
	v_lshl_add_u64 v[48:49], v[18:19], 1, s[24:25]
	v_min_i32_e32 v19, 0x62f, v26
	v_lshlrev_b32_e32 v18, 3, v20
	v_mul_hi_i32 v20, v19, s17
	v_lshrrev_b32_e32 v21, 31, v20
	v_ashrrev_i32_e32 v20, 7, v20
	v_add_u32_e32 v20, v20, v21
	v_mad_i32_i24 v21, v20, s26, v19
	v_lshlrev_b32_e32 v20, 11, v20
	v_ashrrev_i32_e32 v105, 3, v21
	v_ashrrev_i32_e32 v21, 31, v20
	v_lshlrev_b32_e32 v19, 3, v19
	v_lshl_add_u64 v[50:51], v[20:21], 1, s[24:25]
	v_and_b32_e32 v20, 56, v19
	v_min_i32_e32 v19, 0x62f, v27
	v_mul_hi_i32 v21, v19, s17
	v_lshrrev_b32_e32 v26, 31, v21
	v_ashrrev_i32_e32 v21, 7, v21
	v_add_u32_e32 v21, v21, v26
	v_mad_i32_i24 v26, v21, s26, v19
	v_ashrrev_i32_e32 v106, 3, v26
	v_lshlrev_b32_e32 v26, 11, v21
	v_ashrrev_i32_e32 v27, 31, v26
	v_lshlrev_b32_e32 v19, 3, v19
	v_lshl_add_u64 v[52:53], v[26:27], 1, s[24:25]
	v_and_b32_e32 v26, 56, v19
	v_or_b32_e32 v19, 1, v44
	v_mad_u64_u32 v[54:55], s[24:25], v96, s27, v[24:25]
	v_mul_u32_u24_e32 v19, 0x104, v19
	v_and_b32_e32 v18, 56, v18
	v_add3_u32 v55, 0, v19, v23
	v_readlane_b32 s22, v254, 4
	s_mov_b32 s13, -1
	v_add_u32_e32 v97, 0x800, v96
	v_add_u32_e32 v98, 0x1000, v96
	v_add_u32_e32 v107, 0x104, v55
	v_add_u32_e32 v108, 0x208, v55
	v_add_u32_e32 v109, 0x30c, v55
	v_add_u32_e32 v110, 0x410, v55
	v_add_u32_e32 v111, 0x514, v55
	v_add_u32_e32 v112, 0x618, v55
	s_lshl_b32 s17, s22, 1
	s_lshl_b32 s33, s22, 6
	s_mov_b64 s[24:25], 0x6000
	s_mov_b64 s[26:27], 0xc000
	s_mov_b32 s36, 0xc000
	s_movk_i32 s37, 0x6000
	s_movk_i32 s38, 0x2000
	v_add_u32_e32 v113, v24, v25
	v_add_u32_e32 v114, v24, v28
	v_add_u32_e32 v115, v24, v29
	v_add_u32_e32 v116, v24, v30
	v_lshlrev_b32_e32 v56, 1, v22
	v_lshlrev_b32_e32 v58, 1, v18
	v_lshlrev_b32_e32 v60, 1, v20
	v_lshlrev_b32_e32 v62, 1, v26
	v_lshlrev_b32_e32 v42, 1, v44
	s_mov_b32 s39, s28
	v_mov_b32_e32 v68, v43
	v_mov_b32_e32 v69, v43
	v_mov_b32_e32 v64, v43
	v_mov_b32_e32 v65, v43
	v_mov_b32_e32 v66, v43
	v_mov_b32_e32 v67, v43
	v_mov_b32_e32 v70, v43
	v_mov_b32_e32 v71, v43
	s_branch .LBB0_307

; __device__ __forceinline__ void hy_conv_phase(LAS unsigned char* lds, int bid, int G, const bf16_t* u, const float* cw, const float* cb, bf16_t* x0c, bf16_t* vgT) {
;     ...
;         if (c0 != cwc0) { cwc0 = c0;
; #pragma unroll
;             for (int q = 0; q < 8; ++q) { const int cc = c0 + (tid & 7) * 8 + q; wa[q] = cw[cc]; wb[q] = cw[6144 + cc]; wc_[q] = cw[12288 + cc]; wd[q] = cb[cc]; }
;             const int c1 = 2048 + c0 + (tid >> 3), c2 = 4096 + c0 + (tid >> 3);
;             p0 = cw[c1]; p1 = cw[6144 + c1]; p2 = cw[12288 + c1]; pb = cb[c1]; q0 = cw[c2]; q1 = cw[6144 + c2]; q2 = cw[12288 + c2]; qb = cb[c2]; }
.LBB0_307:
	s_and_b32 s41, s29, 0x7c0
	s_cmp_eq_u32 s41, s13
	s_cbranch_scc1 .LBB0_309
	v_or_b32_e32 v18, s41, v44
	v_lshlrev_b32_e32 v34, 2, v18
	v_mov_b32_e32 v35, v43
	v_lshl_add_u64 v[18:19], s[8:9], 0, v[34:35]
	v_add_co_u32_e32 v22, vcc, s36, v18
	v_add_u32_e32 v40, s41, v97
	s_nop 0
	v_addc_co_u32_e32 v23, vcc, 0, v19, vcc
	v_ashrrev_i32_e32 v41, 31, v40
	v_add_co_u32_e32 v38, vcc, s37, v18
	v_lshlrev_b64 v[40:41], 2, v[40:41]
	s_nop 0
	v_addc_co_u32_e32 v39, vcc, 0, v19, vcc
	v_lshl_add_u64 v[64:65], s[8:9], 0, v[40:41]
	v_add_co_u32_e32 v66, vcc, s37, v64
	v_add_u32_e32 v72, s41, v98
	s_nop 0
	v_addc_co_u32_e32 v67, vcc, 0, v65, vcc
	v_lshl_add_u64 v[20:21], v[18:19], 0, s[24:25]
	v_lshl_add_u64 v[26:27], v[18:19], 0, s[26:27]
	v_add_co_u32_e32 v68, vcc, s36, v64
	v_lshl_add_u64 v[40:41], s[10:11], 0, v[40:41]
	v_ashrrev_i32_e32 v73, 31, v72
	global_load_dwordx4 v[22:25], v[22:23], off nt
	s_nop 0
	global_load_dwordx4 v[30:33], v[26:27], off offset:16 nt
	s_nop 0
	global_load_dwordx4 v[18:21], v[20:21], off offset:16 nt
	s_nop 0
	global_load_dwordx4 v[76:79], v34, s[8:9] offset:16 nt
	global_load_dwordx4 v[26:29], v34, s[10:11] offset:16 nt
	global_load_dwordx4 v[118:121], v34, s[8:9] nt
	s_nop 0
	global_load_dwordx4 v[34:37], v34, s[10:11] nt
	v_addc_co_u32_e32 v69, vcc, 0, v65, vcc
	global_load_dword v64, v[64:65], off
	s_nop 0
	global_load_dword v66, v[66:67], off
	s_nop 0
	global_load_dword v70, v[68:69], off
	s_mov_b32 s13, s41
	global_load_dword v68, v[40:41], off
	v_lshlrev_b64 v[40:41], 2, v[72:73]
	v_lshl_add_u64 v[72:73], s[8:9], 0, v[40:41]
	v_add_co_u32_e32 v74, vcc, s37, v72
	v_lshl_add_u64 v[40:41], s[10:11], 0, v[40:41]
	s_nop 0
	v_addc_co_u32_e32 v75, vcc, 0, v73, vcc
	v_add_co_u32_e32 v80, vcc, s36, v72
	s_waitcnt vmcnt(9)
	v_mov_b32_e32 v83, v32
	v_addc_co_u32_e32 v81, vcc, 0, v73, vcc
	global_load_dword v65, v[72:73], off
	global_load_dword v67, v[74:75], off
	global_load_dword v71, v[80:81], off
	global_load_dword v69, v[40:41], off
	s_nop 0
	global_load_dwordx4 v[38:41], v[38:39], off nt
	s_waitcnt vmcnt(12)
	v_mov_b32_e32 v82, v78
	v_mov_b32_e32 v80, v79
	v_mov_b32_e32 v86, v76
	v_mov_b32_e32 v84, v77
	s_waitcnt vmcnt(10)
	v_mov_b32_e32 v90, v120
	v_mov_b32_e32 v88, v121
	v_mov_b32_e32 v94, v118
	v_mov_b32_e32 v92, v119
	v_mov_b32_e32 v72, v78
	v_mov_b32_e32 v74, v76
	v_mov_b32_e32 v76, v120
	v_mov_b32_e32 v78, v118
	v_mov_b32_e32 v81, v33
	v_mov_b32_e32 v87, v30
	v_mov_b32_e32 v85, v31
	v_mov_b32_e32 v73, v32
	v_mov_b32_e32 v32, v79
	v_mov_b32_e32 v75, v30
	v_mov_b32_e32 v30, v77
	v_mov_b32_e32 v91, v24
	v_mov_b32_e32 v89, v25
	v_mov_b32_e32 v95, v22
	v_mov_b32_e32 v93, v23
	v_mov_b32_e32 v77, v24
	v_mov_b32_e32 v24, v121
	v_mov_b32_e32 v79, v22
	v_mov_b32_e32 v22, v119
	s_branch .LBB0_310

; __device__ __forceinline__ void hy_conv_phase(LAS unsigned char* lds, int bid, int G, const bf16_t* u, const float* cw, const float* cb, bf16_t* x0c, bf16_t* vgT) {
;     ...
;         if (tile + G < 4096) HC_LOAD(tile + G, pv);
.LBB0_320:
	s_andn2_b64 vcc, exec, s[34:35]
	s_cbranch_vccnz .LBB0_306
	s_add_i32 s42, s17, s40
	s_and_b32 s22, s42, 0xffffffc0
	s_add_i32 s34, s22, -1
	s_waitcnt vmcnt(3)
	v_add_u32_e32 v2, s34, v1
	v_add_u32_e32 v4, s34, v104
	s_waitcnt vmcnt(1)
	v_add_u32_e32 v10, s34, v105
	v_add_u32_e32 v12, s34, v106
	s_add_i32 s43, s33, s29
	v_med3_i32 v2, v2, 0, v45
	v_med3_i32 v4, v4, 0, v45
	v_med3_i32 v10, v10, 0, v45
	v_med3_i32 v12, v12, 0, v45
	s_and_b32 s29, s43, 0x7c0
	v_mul_u32_u24_e32 v2, 0x1800, v2
	v_mov_b32_e32 v3, v43
	v_mul_u32_u24_e32 v4, 0x1800, v4
	v_mov_b32_e32 v5, v43
	v_mul_u32_u24_e32 v10, 0x1800, v10
	v_mov_b32_e32 v11, v43
	v_mul_u32_u24_e32 v12, 0x1800, v12
	v_mov_b32_e32 v13, v43
	v_lshl_add_u64 v[2:3], v[2:3], 1, v[46:47]
	s_lshl_b32 s22, s29, 1
	v_lshl_add_u64 v[4:5], v[4:5], 1, v[48:49]
	v_lshl_add_u64 v[10:11], v[10:11], 1, v[50:51]
	v_lshl_add_u64 v[12:13], v[12:13], 1, v[52:53]
	v_lshl_add_u64 v[2:3], v[2:3], 0, s[22:23]
	v_mov_b32_e32 v57, v43
	v_lshl_add_u64 v[4:5], v[4:5], 0, s[22:23]
	v_mov_b32_e32 v59, v43
	v_lshl_add_u64 v[10:11], v[10:11], 0, s[22:23]
	v_mov_b32_e32 v61, v43
	v_lshl_add_u64 v[12:13], v[12:13], 0, s[22:23]
	v_mov_b32_e32 v63, v43
	v_lshl_add_u64 v[2:3], v[2:3], 0, v[56:57]
	v_lshl_add_u64 v[6:7], v[4:5], 0, v[58:59]
	v_lshl_add_u64 v[10:11], v[10:11], 0, v[60:61]
	s_waitcnt vmcnt(0)
	v_lshl_add_u64 v[14:15], v[12:13], 0, v[62:63]
	global_load_dwordx4 v[2:5], v[2:3], off nt
	s_nop 0
	global_load_dwordx4 v[6:9], v[6:7], off nt
	s_nop 0
	global_load_dwordx4 v[10:13], v[10:11], off nt
	s_nop 0
	global_load_dwordx4 v[14:17], v[14:15], off nt
	s_branch .LBB0_306

; #define LAS __attribute__((address_space(3)))
; __device__ __forceinline__ int tid_fresh() { int t = threadIdx.x; asm volatile("" : "+v"(t)); return t; }
; #define HT_LOAD(tile_) do { const int t0_ = ((tile_) >> 5) * 64, c0_ = ((tile_) & 31) * 64; pz = *(const u32x4*)(zT + (size_t)(c0_ + c) * T + t0_ + tc * 8); px = *(const u32x4*)(x0c + (size_t)(t0_ + t) * D + c0_ + ch * 8); } while (0)
; __device__ __forceinline__ void hy_tr_phase(LAS unsigned char* lds, int bid, int G, const bf16_t* zT, const bf16_t* x0c, bf16_t* yA) {
;     LAS float* sm = (LAS float*)lds;
;     const int tid = tid_fresh();
;     const int c = tid >> 3, tc = tid & 7, t = tid >> 3, ch = tid & 7;
;     ...
;     u32x4 pz = (u32x4){0u, 0u, 0u, 0u}, px = (u32x4){0u, 0u, 0u, 0u};
;     if (bid < 4096) HT_LOAD(bid);
.LBB0_869:
	s_or_b64 exec, exec, s[0:1]
	v_readlane_b32 s0, v254, 0
	v_readlane_b32 s1, v254, 1
	v_mov_b32_e32 v2, v0
	s_and_b64 vcc, exec, s[18:19]
	s_waitcnt lgkmcnt(0)
	s_barrier
	s_cbranch_vccz .LBB0_876
	s_load_dwordx2 s[4:5], s[0:1], 0x118
	v_readlane_b32 s6, v254, 19
	s_mov_b32 s16, s6
	v_readlane_b32 s7, v254, 20
	v_ashrrev_i32_e32 v1, 3, v2
	s_waitcnt lgkmcnt(0)
	s_add_u32 s0, s4, 0x43650000
	s_addc_u32 s1, s5, 0
	s_add_u32 s2, s4, 0x49a50000
	s_addc_u32 s3, s5, 0
	s_add_u32 s4, s4, 0x34c30000
	s_addc_u32 s5, s5, 0
	s_lshl_b32 s12, s6, 6
	s_and_b32 s14, s12, 0x7c0
	s_lshl_b32 s6, s14, 1
	s_add_u32 s6, s2, s6
	s_addc_u32 s7, s3, 0
	s_lshl_b32 s13, s16, 1
	s_and_b32 s8, s13, 0xffffffc0
	s_ashr_i32 s9, s8, 31
	v_and_b32_e32 v17, 7, v2
	s_lshl_b64 s[10:11], s[8:9], 1
	v_add_u32_e32 v2, s14, v1
	s_add_u32 s10, s0, s10
	v_ashrrev_i32_e32 v3, 31, v2
	s_addc_u32 s11, s1, s11
	v_lshlrev_b64 v[2:3], 14, v[2:3]
	v_lshl_add_u64 v[2:3], s[10:11], 0, v[2:3]
	v_mov_b32_e32 v15, 0
	v_lshlrev_b32_e32 v14, 4, v17
	v_lshl_add_u64 v[10:11], v[2:3], 0, v[14:15]
	v_add_u32_e32 v2, s8, v1
	v_ashrrev_i32_e32 v3, 31, v2
	v_lshlrev_b64 v[2:3], 12, v[2:3]
	v_lshl_add_u64 v[2:3], s[6:7], 0, v[2:3]
	v_lshl_add_u64 v[12:13], v[2:3], 0, v[14:15]
	global_load_dwordx4 v[6:9], v[10:11], off nt
	global_load_dwordx4 v[2:5], v[12:13], off nt
	v_lshl_add_u32 v11, v1, 2, 0
	v_lshlrev_b32_e32 v12, 8, v1
	v_lshlrev_b32_e32 v13, 5, v17
	v_add3_u32 v16, v11, v12, v13
	v_mul_u32_u24_e32 v12, 0x820, v17
	v_lshlrev_b32_e32 v10, 3, v17
	v_readlane_b32 s6, v254, 4
	v_add_u32_e32 v17, v11, v12
	s_mov_b32 s7, 0
	s_lshl_b32 s14, s6, 1
	s_lshl_b32 s15, s6, 6
	v_lshlrev_b32_e32 v14, 1, v10
	v_add_u32_e32 v18, 0x400, v17
	s_branch .LBB0_872

; #define LAS __attribute__((address_space(3)))
; __device__ __forceinline__ float bf_lo(unsigned w) { return __uint_as_float(w << 16); }
; __device__ __forceinline__ float bf_hi(unsigned w) { return __uint_as_float(w & 0xffff0000u); }
; #define HT_LOAD(tile_) do { const int t0_ = ((tile_) >> 5) * 64, c0_ = ((tile_) & 31) * 64; pz = *(const u32x4*)(zT + (size_t)(c0_ + c) * T + t0_ + tc * 8); px = *(const u32x4*)(x0c + (size_t)(t0_ + t) * D + c0_ + ch * 8); } while (0)
; __device__ __forceinline__ void hy_tr_phase(LAS unsigned char* lds, int bid, int G, const bf16_t* zT, const bf16_t* x0c, bf16_t* yA) {
;     ...
;     for (int tile = bid; tile < 4096; tile += G) {
;         const int t0 = (tile >> 5) * 64, c0 = (tile & 31) * 64;
;         __syncthreads();
;         {   LAS float* dp = sm + c * 65 + tc * 8; dp[0] = bf_lo(pz.x); dp[1] = bf_hi(pz.x); dp[2] = bf_lo(pz.y); dp[3] = bf_hi(pz.y); dp[4] = bf_lo(pz.z); dp[5] = bf_hi(pz.z); dp[6] = bf_lo(pz.w); dp[7] = bf_hi(pz.w); }
;         const u32x4 xv = px;
;         if (tile + G < 4096) HT_LOAD(tile + G);
.LBB0_874:
	s_waitcnt vmcnt(0)
	v_mov_b64_e32 v[12:13], v[4:5]
	s_andn2_b64 vcc, exec, s[10:11]
	v_mov_b64_e32 v[10:11], v[2:3]
	s_cbranch_vccnz .LBB0_871
	s_add_i32 s18, s15, s12
	s_and_b32 s6, s18, 0x7c0
	v_add_u32_e32 v6, s6, v1
	s_add_i32 s17, s14, s13
	v_ashrrev_i32_e32 v7, 31, v6
	s_and_b32 s10, s17, 0xffffffc0
	v_lshlrev_b64 v[6:7], 14, v[6:7]
	v_lshl_add_u64 v[6:7], s[0:1], 0, v[6:7]
	s_ashr_i32 s11, s10, 31
	v_lshl_add_u64 v[6:7], s[10:11], 1, v[6:7]
	v_lshl_add_u64 v[20:21], v[6:7], 0, v[14:15]
	v_add_u32_e32 v6, s10, v1
	v_ashrrev_i32_e32 v7, 31, v6
	v_lshlrev_b64 v[6:7], 12, v[6:7]
	v_lshl_add_u64 v[6:7], s[2:3], 0, v[6:7]
	s_lshl_b32 s6, s6, 1
	v_lshl_add_u64 v[6:7], v[6:7], 0, s[6:7]
	v_lshl_add_u64 v[22:23], v[6:7], 0, v[14:15]
	global_load_dwordx4 v[6:9], v[20:21], off nt
	global_load_dwordx4 v[10:13], v[22:23], off nt
	s_branch .LBB0_871

; __device__ __forceinline__ void row_norm_mod2(float4 (&v0)[8], float4 (&v1)[8], int lane, const float* g, const float* sc, const float* sh) {
;     float4 ga[8], s1a[8];
; #pragma unroll
;     for (int i = 0; i < 8; ++i) { const int c = (lane + 64 * i) * 4; ga[i] = *(const float4*)(g + c); s1a[i] = *(const float4*)(sc + c); }
;     float ssa = 0.f, ssb = 0.f;
; #pragma unroll
;     for (int i = 0; i < 8; ++i) { ssa += v0[i].x * v0[i].x + v0[i].y * v0[i].y + v0[i].z * v0[i].z + v0[i].w * v0[i].w; ssb += v1[i].x * v1[i].x + v1[i].y * v1[i].y + v1[i].z * v1[i].z + v1[i].w * v1[i].w; }
; __device__ __forceinline__ void route_phase(LAS unsigned char* lds, int bid, int G, const float* x, const float* g, const float* sc, const float* sh,
;                                             const float* rw, const float* rbias, bf16_t* hbuf, int* cnt, int* list, u32x2* rec) {
;     ...
;         {   const int row = r0 + wave * 2;
;             float4 va[8], vb[8];
; #pragma unroll
;             for (int i = 0; i < 8; ++i) { va[i] = *(const float4*)(x + (size_t)row * D + (lane + 64 * i) * 4); vb[i] = *(const float4*)(x + (size_t)(row + 1) * D + (lane + 64 * i) * 4); }
;             row_norm_mod2(va, vb, lane, g, sc, sh);
.LBB0_1003:
	v_mov_b32_e32 v1, v0
	v_readlane_b32 s2, v254, 29
	v_ashrrev_i32_e32 v166, 6, v1
	v_lshlrev_b32_e32 v160, 1, v166
	v_add_u32_e32 v46, s33, v160
	v_and_b32_e32 v159, 63, v1
	v_ashrrev_i32_e32 v47, 31, v46
	v_lshlrev_b32_e32 v130, 4, v159
	v_lshlrev_b64 v[2:3], 13, v[46:47]
	v_mov_b32_e32 v59, v131
	v_or_b32_e32 v58, 0x1000, v130
	v_lshl_add_u64 v[26:27], s[68:69], 0, v[2:3]
	v_readlane_b32 s3, v254, 30
	v_mov_b32_e32 v139, v131
	v_or_b32_e32 v138, 0x1400, v130
	v_lshl_add_u64 v[10:11], v[26:27], 0, v[58:59]
	s_barrier
	s_nop 0
	global_load_dwordx4 v[42:45], v130, s[2:3] nt
	v_lshl_add_u64 v[12:13], v[26:27], 0, v[138:139]
	global_load_dwordx4 v[2:5], v[10:11], off nt
	global_load_dwordx4 v[6:9], v[12:13], off nt
	v_mov_b32_e32 v143, v131
	v_or_b32_e32 v142, 0x1800, v130
	v_mov_b32_e32 v141, v131
	v_or_b32_e32 v140, 0x1c00, v130
	v_lshl_add_u64 v[18:19], v[26:27], 0, v[142:143]
	v_or_b32_e32 v48, 1, v46
	v_lshl_add_u64 v[20:21], v[26:27], 0, v[140:141]
	global_load_dwordx4 v[14:17], v[18:19], off nt
	global_load_dwordx4 v[10:13], v[20:21], off nt
	v_ashrrev_i32_e32 v49, 31, v48
	v_lshlrev_b64 v[18:19], 13, v[48:49]
	v_lshl_add_u64 v[50:51], s[68:69], 0, v[18:19]
	v_lshl_add_u64 v[28:29], v[50:51], 0, v[58:59]
	v_lshl_add_u64 v[30:31], v[50:51], 0, v[138:139]
	s_waitcnt lgkmcnt(0)
	global_load_dwordx4 v[22:25], v[28:29], off nt
	global_load_dwordx4 v[18:21], v[30:31], off nt
	v_cmp_lt_i32_e32 vcc, v150, v149
	v_lshl_add_u64 v[78:79], v[50:51], 0, v[130:131]
	v_lshl_add_u64 v[54:55], v[26:27], 0, v[130:131]
	v_cndmask_b32_e32 v32, v133, v150, vcc
	v_cmp_lt_i32_e32 vcc, v151, v149
	global_load_dwordx4 v[38:41], v[78:79], off nt
	global_load_dwordx4 v[82:85], v[54:55], off nt
	v_cndmask_b32_e32 v33, v133, v151, vcc
	v_cmp_lt_i32_e32 vcc, v152, v149
	s_movk_i32 s0, 0x4010
	v_mul_lo_u32 v26, v166, s0
	v_cndmask_b32_e32 v34, v133, v152, vcc
	v_cmp_lt_i32_e32 vcc, v153, v149
	v_readlane_b32 s8, v254, 31
	v_readlane_b32 s0, v254, 27
	v_cndmask_b32_e32 v35, v133, v153, vcc
	v_cmp_lt_i32_e32 vcc, v154, v149
	v_readlane_b32 s9, v254, 32
	v_readlane_b32 s1, v254, 28
	v_cndmask_b32_e32 v36, v133, v154, vcc
	v_cmp_lt_i32_e32 vcc, v155, v149
	v_lshlrev_b32_e32 v139, 2, v32
	v_lshlrev_b32_e32 v161, 2, v33
	v_cndmask_b32_e32 v37, v133, v155, vcc
	v_lshlrev_b32_e32 v162, 2, v34
	v_lshlrev_b32_e32 v163, 2, v35
	v_lshlrev_b32_e32 v164, 2, v36
	v_lshlrev_b32_e32 v165, 2, v37
	v_add3_u32 v167, 0, v26, v130
	global_load_dwordx4 v[26:29], v130, s[8:9] nt
	global_load_dwordx4 v[34:37], v130, s[0:1] nt
	global_load_dwordx4 v[30:33], v130, s[0:1] offset:1024 nt
	global_load_dwordx4 v[66:69], v[78:79], off offset:1024 nt
	global_load_dwordx4 v[86:89], v[54:55], off offset:1024 nt
	global_load_dwordx4 v[90:93], v[54:55], off offset:2048 nt
	global_load_dwordx4 v[74:77], v[78:79], off offset:2048 nt
	v_readlane_b32 s10, v254, 33
	v_lshlrev_b64 v[46:47], 12, v[46:47]
	v_readlane_b32 s11, v254, 34
	v_lshlrev_b64 v[48:49], 12, v[48:49]
	v_mov_b32_e32 v53, v131
	v_lshlrev_b32_e32 v52, 3, v159
	v_or_b32_e32 v56, 0x400, v130
	v_or_b32_e32 v57, 0x800, v130
	v_or_b32_e32 v59, 0xc00, v130
	v_lshl_add_u64 v[46:47], s[10:11], 0, v[46:47]
	v_lshl_add_u64 v[48:49], s[10:11], 0, v[48:49]
	v_lshl_add_u64 v[136:137], v[46:47], 0, v[52:53]
	v_lshl_add_u64 v[98:99], v[50:51], 0, v[142:143]
	v_lshl_add_u64 v[102:103], v[50:51], 0, v[140:141]
	v_lshl_add_u64 v[134:135], v[48:49], 0, v[52:53]
	v_add_u32_e32 v202, 0x2008, v167
	v_add_u32_e32 v203, 0x2808, v167
	v_add_u32_e32 v204, 0x2c08, v167
	v_add_u32_e32 v205, 0x3008, v167
	v_add_u32_e32 v206, 0x3408, v167
	v_add_u32_e32 v207, 0x3808, v167
	s_waitcnt vmcnt(15)
	v_pk_add_f32 v[146:147], v[42:43], 1.0 op_sel_hi:[1,0]
	v_pk_add_f32 v[144:145], v[44:45], 1.0 op_sel_hi:[1,0]
	global_load_dwordx4 v[168:171], v56, s[2:3] nt
	global_load_dwordx4 v[50:53], v56, s[8:9] nt
	global_load_dwordx4 v[126:129], v57, s[2:3] nt
	global_load_dwordx4 v[42:45], v57, s[8:9] nt
	global_load_dwordx4 v[94:97], v[54:55], off offset:3072 nt
	global_load_dwordx4 v[70:73], v130, s[0:1] offset:2048 nt
	s_nop 0
	global_load_dwordx4 v[54:57], v130, s[0:1] offset:3072 nt
	global_load_dwordx4 v[118:121], v59, s[2:3] nt
	global_load_dwordx4 v[62:65], v59, s[8:9] nt
	global_load_dwordx4 v[46:49], v58, s[0:1] nt
	global_load_dwordx4 v[110:113], v58, s[2:3] nt
	s_nop 0
	global_load_dwordx4 v[58:61], v58, s[8:9] nt
	s_nop 0
	global_load_dwordx4 v[78:81], v[78:79], off offset:3072 nt
	s_nop 0
	global_load_dwordx4 v[114:117], v138, s[2:3] nt
	s_waitcnt vmcnt(28)
	v_mov_b32_e32 v104, v3
	s_waitcnt vmcnt(27)
	v_mov_b32_e32 v105, v7
	v_mov_b32_e32 v100, v2
	v_mov_b32_e32 v101, v6
	v_pk_mul_f32 v[104:105], v[104:105], v[104:105]
	v_mov_b32_e32 v106, v5
	v_pk_fma_f32 v[100:101], v[100:101], v[100:101], v[104:105]
	v_mov_b32_e32 v104, v4
	v_mov_b32_e32 v105, v8
	v_mov_b32_e32 v107, v9
	v_pk_fma_f32 v[100:101], v[104:105], v[104:105], v[100:101]
	s_waitcnt vmcnt(26)
	v_mov_b32_e32 v176, v15
	v_pk_fma_f32 v[172:173], v[106:107], v[106:107], v[100:101]
	global_load_dwordx4 v[122:125], v142, s[2:3] nt
	global_load_dwordx4 v[106:109], v140, s[2:3] nt
	s_nop 0
	global_load_dwordx4 v[98:101], v[98:99], off nt
	s_nop 0
	global_load_dwordx4 v[102:105], v[102:103], off nt
	s_waitcnt vmcnt(29)
	v_mov_b32_e32 v177, v11
	v_mov_b32_e32 v174, v14
	v_mov_b32_e32 v175, v10
	v_pk_mul_f32 v[176:177], v[176:177], v[176:177]
	v_mov_b32_e32 v178, v17
	v_pk_fma_f32 v[174:175], v[174:175], v[174:175], v[176:177]
	v_mov_b32_e32 v176, v16
	v_mov_b32_e32 v177, v12
	v_mov_b32_e32 v179, v13
	v_pk_fma_f32 v[174:175], v[176:177], v[176:177], v[174:175]
	s_waitcnt vmcnt(28)
; __device__ __forceinline__ void row_norm_mod2(float4 (&v0)[8], float4 (&v1)[8], int lane, const float* g, const float* sc, const float* sh) {
;     ...
;     float ssa = 0.f, ssb = 0.f;
; #pragma unroll
;     for (int i = 0; i < 8; ++i) { ssa += v0[i].x * v0[i].x + v0[i].y * v0[i].y + v0[i].z * v0[i].z + v0[i].w * v0[i].w; ssb += v1[i].x * v1[i].x + v1[i].y * v1[i].y + v1[i].z * v1[i].z + v1[i].w * v1[i].w; }
;     ssa = wave_sum(ssa); ssb = wave_sum(ssb);
;     const float ra = rsqrtf(ssa * (1.f / D) + EPS), rb = rsqrtf(ssb * (1.f / D) + EPS);
; #pragma unroll
;     for (int i = 0; i < 8; ++i) { const int c = (lane + 64 * i) * 4; const float4 gg = ga[i], s1 = s1a[i], s0 = *(const float4*)(sh + c);
	v_mov_b32_e32 v176, v22
	v_pk_fma_f32 v[174:175], v[178:179], v[178:179], v[174:175]
	v_mov_b32_e32 v178, v23
	s_waitcnt vmcnt(27)
	v_mov_b32_e32 v179, v19
	v_mov_b32_e32 v177, v18
	v_pk_mul_f32 v[178:179], v[178:179], v[178:179]
	v_mov_b32_e32 v180, v25
	v_pk_fma_f32 v[176:177], v[176:177], v[176:177], v[178:179]
	v_mov_b32_e32 v178, v24
	v_mov_b32_e32 v179, v20
	v_mov_b32_e32 v181, v21
	v_pk_fma_f32 v[176:177], v[178:179], v[178:179], v[176:177]
	s_waitcnt vmcnt(26)
	v_mov_b32_e32 v178, v38
	v_pk_fma_f32 v[176:177], v[180:181], v[180:181], v[176:177]
	v_mov_b32_e32 v180, v39
	s_waitcnt vmcnt(25)
	v_mov_b32_e32 v181, v83
	v_mov_b32_e32 v179, v82
	v_pk_mul_f32 v[180:181], v[180:181], v[180:181]
	v_mov_b32_e32 v182, v41
	v_pk_fma_f32 v[178:179], v[178:179], v[178:179], v[180:181]
	v_mov_b32_e32 v180, v40
	v_mov_b32_e32 v181, v84
	v_mov_b32_e32 v183, v85
	v_pk_fma_f32 v[178:179], v[180:181], v[180:181], v[178:179]
	s_waitcnt vmcnt(21)
	v_mov_b32_e32 v180, v66
	v_pk_fma_f32 v[178:179], v[182:183], v[182:183], v[178:179]
	v_mov_b32_e32 v182, v67
	s_waitcnt vmcnt(20)
	v_mov_b32_e32 v183, v87
	v_mov_b32_e32 v181, v86
	v_pk_mul_f32 v[182:183], v[182:183], v[182:183]
	v_mov_b32_e32 v184, v69
	v_pk_fma_f32 v[180:181], v[180:181], v[180:181], v[182:183]
	v_mov_b32_e32 v182, v68
	v_mov_b32_e32 v183, v88
	v_mov_b32_e32 v185, v89
	v_pk_fma_f32 v[180:181], v[182:183], v[182:183], v[180:181]
	s_waitcnt vmcnt(18)
	v_mov_b32_e32 v182, v75
	v_pk_fma_f32 v[180:181], v[184:185], v[184:185], v[180:181]
	v_mov_b32_e32 v183, v91
	v_pk_add_f32 v[178:179], v[178:179], v[180:181]
	v_mov_b32_e32 v180, v74
	v_mov_b32_e32 v181, v90
	v_pk_mul_f32 v[182:183], v[182:183], v[182:183]
	v_mov_b32_e32 v184, v77
	v_pk_fma_f32 v[180:181], v[180:181], v[180:181], v[182:183]
	v_mov_b32_e32 v182, v76
	v_mov_b32_e32 v183, v92
	v_mov_b32_e32 v185, v93
	v_pk_fma_f32 v[180:181], v[182:183], v[182:183], v[180:181]
	s_waitcnt vmcnt(13)
	v_mov_b32_e32 v183, v95
	v_pk_fma_f32 v[180:181], v[184:185], v[184:185], v[180:181]
	v_mov_b32_e32 v185, v97
	v_pk_add_f32 v[178:179], v[178:179], v[180:181]
	v_mov_b32_e32 v181, v94
	s_waitcnt vmcnt(5)
	v_mov_b32_e32 v182, v79
	v_mov_b32_e32 v180, v78
	v_pk_mul_f32 v[182:183], v[182:183], v[182:183]
	v_mov_b32_e32 v184, v81
	v_pk_fma_f32 v[180:181], v[180:181], v[180:181], v[182:183]
	v_mov_b32_e32 v182, v80
	v_mov_b32_e32 v183, v96
	v_pk_fma_f32 v[180:181], v[182:183], v[182:183], v[180:181]
	v_pk_add_f32 v[188:189], v[168:169], 1.0 op_sel_hi:[1,0]
	v_pk_fma_f32 v[180:181], v[184:185], v[184:185], v[180:181]
	v_pk_add_f32 v[190:191], v[170:171], 1.0 op_sel_hi:[1,0]
	v_pk_add_f32 v[178:179], v[178:179], v[180:181]
	v_mov_b32_e32 v180, v176
	v_mov_b32_e32 v181, v172
	s_waitcnt vmcnt(1)
	v_mov_b32_e32 v182, v99
	s_waitcnt vmcnt(0)
	v_mov_b32_e32 v183, v103
	v_pk_add_f32 v[178:179], v[178:179], v[180:181]
	v_mov_b32_e32 v180, v98
	v_mov_b32_e32 v181, v102
	v_pk_mul_f32 v[182:183], v[182:183], v[182:183]
	v_mov_b32_e32 v184, v101
	v_pk_fma_f32 v[180:181], v[180:181], v[180:181], v[182:183]
	v_mov_b32_e32 v182, v100
	v_mov_b32_e32 v183, v104
	v_mov_b32_e32 v185, v105
	v_pk_fma_f32 v[180:181], v[182:183], v[182:183], v[180:181]
	v_mov_b32_e32 v172, v177
	v_pk_fma_f32 v[180:181], v[184:185], v[184:185], v[180:181]
	v_pk_add_f32 v[172:173], v[178:179], v[172:173]
	v_mov_b32_e32 v176, v180
	v_mov_b32_e32 v177, v174
	v_pk_add_f32 v[172:173], v[172:173], v[176:177]
	v_mov_b32_e32 v174, v181
	v_pk_add_f32 v[180:181], v[172:173], v[174:175]
	ds_bpermute_b32 v183, v139, v181
	ds_bpermute_b32 v182, v139, v180
	global_load_dwordx4 v[172:175], v138, s[0:1] nt
	global_load_dwordx4 v[176:179], v138, s[8:9] nt
	v_pk_add_f32 v[196:197], v[110:111], 1.0 op_sel_hi:[1,0]
	v_pk_add_f32 v[198:199], v[106:107], 1.0 op_sel_hi:[1,0]
	v_pk_add_f32 v[200:201], v[108:109], 1.0 op_sel_hi:[1,0]
	s_waitcnt lgkmcnt(0)
	v_pk_add_f32 v[192:193], v[180:181], v[182:183]
	global_load_dwordx4 v[168:171], v142, s[0:1] nt
	global_load_dwordx4 v[180:183], v142, s[8:9] nt
	global_load_dwordx4 v[184:187], v140, s[0:1] nt
	ds_bpermute_b32 v195, v161, v193
	global_load_dwordx4 v[140:143], v140, s[8:9] nt
	ds_bpermute_b32 v194, v161, v192
	s_mov_b32 s0, 0x3a000000
	v_pk_add_f32 v[114:115], v[114:115], 1.0 op_sel_hi:[1,0]
	v_pk_add_f32 v[116:117], v[116:117], 1.0 op_sel_hi:[1,0]
	v_pk_add_f32 v[122:123], v[122:123], 1.0 op_sel_hi:[1,0]
	s_waitcnt lgkmcnt(0)
	v_pk_add_f32 v[192:193], v[192:193], v[194:195]
	ds_bpermute_b32 v195, v162, v193
	ds_bpermute_b32 v194, v162, v192
	v_pk_add_f32 v[124:125], v[124:125], 1.0 op_sel_hi:[1,0]
	v_pk_add_f32 v[126:127], v[126:127], 1.0 op_sel_hi:[1,0]
	v_pk_add_f32 v[128:129], v[128:129], 1.0 op_sel_hi:[1,0]
	v_add_u32_e32 v138, 0x2408, v167
	s_waitcnt lgkmcnt(0)
	v_pk_add_f32 v[192:193], v[192:193], v[194:195]
	ds_bpermute_b32 v195, v163, v193
	ds_bpermute_b32 v194, v163, v192
	v_pk_add_f32 v[118:119], v[118:119], 1.0 op_sel_hi:[1,0]
	v_pk_add_f32 v[120:121], v[120:121], 1.0 op_sel_hi:[1,0]
	s_waitcnt lgkmcnt(0)
	v_pk_add_f32 v[110:111], v[192:193], v[194:195]
	ds_bpermute_b32 v193, v164, v111
	ds_bpermute_b32 v192, v164, v110
	v_pk_add_f32 v[194:195], v[112:113], 1.0 op_sel_hi:[1,0]
	s_waitcnt lgkmcnt(0)
	v_pk_add_f32 v[110:111], v[110:111], v[192:193]
	ds_bpermute_b32 v113, v165, v111
	ds_bpermute_b32 v112, v165, v110
	s_waitcnt lgkmcnt(0)
; #define LAS __attribute__((address_space(3)))
; __device__ __forceinline__ unsigned cvt_pk_bf16(float lo, float hi) { unsigned r; asm volatile("v_cvt_pk_bf16_f32 %0, %1, %2" : "=v"(r) : "v"(lo), "v"(hi)); return r; }
; __device__ __forceinline__ void row_norm_mod2(float4 (&v0)[8], float4 (&v1)[8], int lane, const float* g, const float* sc, const float* sh) {
;     ...
;     const float ra = rsqrtf(ssa * (1.f / D) + EPS), rb = rsqrtf(ssb * (1.f / D) + EPS);
; #pragma unroll
;     for (int i = 0; i < 8; ++i) { const int c = (lane + 64 * i) * 4; const float4 gg = ga[i], s1 = s1a[i], s0 = *(const float4*)(sh + c);
;         v0[i].x = v0[i].x * ra * gg.x * (1.f + s1.x) + s0.x; v0[i].y = v0[i].y * ra * gg.y * (1.f + s1.y) + s0.y; v0[i].z = v0[i].z * ra * gg.z * (1.f + s1.z) + s0.z; v0[i].w = v0[i].w * ra * gg.w * (1.f + s1.w) + s0.w;
;         v1[i].x = v1[i].x * rb * gg.x * (1.f + s1.x) + s0.x; v1[i].y = v1[i].y * rb * gg.y * (1.f + s1.y) + s0.y; v1[i].z = v1[i].z * rb * gg.z * (1.f + s1.z) + s0.z; v1[i].w = v1[i].w * rb * gg.w * (1.f + s1.w) + s0.w; }
; __device__ __forceinline__ void route_phase(LAS unsigned char* lds, int bid, int G, const float* x, const float* g, const float* sc, const float* sh,
;                                             const float* rw, const float* rbias, bf16_t* hbuf, int* cnt, int* list, u32x2* rec) {
;     ...
;             for (int i = 0; i < 8; ++i) { const int c = (lane + 64 * i) * 4;
;                 u32x2 w; w.x = cvt_pk_bf16(va[i].x, va[i].y); w.y = cvt_pk_bf16(va[i].z, va[i].w); *(u32x2*)(hbuf + (size_t)row * D + c) = w;
;                 u32x2 w2; w2.x = cvt_pk_bf16(vb[i].x, vb[i].y); w2.y = cvt_pk_bf16(vb[i].z, vb[i].w); *(u32x2*)(hbuf + (size_t)(row + 1) * D + c) = w2;
;                 LAS float* hp = hfs + (wave * 2) * HFS_LD + c; hp[0] = va[i].x; hp[1] = va[i].y; hp[2] = va[i].z; hp[3] = va[i].w;
;                 hp[HFS_LD] = vb[i].x; hp[HFS_LD + 1] = vb[i].y; hp[HFS_LD + 2] = vb[i].z; hp[HFS_LD + 3] = vb[i].w; }
	v_pk_add_f32 v[110:111], v[110:111], v[112:113]
	s_nop 0
	v_pk_fma_f32 v[192:193], v[110:111], s[0:1], v[132:133] op_sel_hi:[1,0,0]
	s_mov_b32 s0, 0x800000
	v_mul_f32_e32 v110, 0x4b800000, v193
	v_cmp_gt_f32_e32 vcc, s0, v193
	s_nop 1
	v_cndmask_b32_e32 v110, v193, v110, vcc
	v_rsq_f32_e32 v110, v110
	v_add_u32_e32 v193, 0x3c08, v167
	v_mul_f32_e32 v106, 0x45800000, v110
	v_cndmask_b32_e32 v130, v110, v106, vcc
	v_pk_mul_f32 v[2:3], v[2:3], v[130:131] op_sel_hi:[1,0]
	v_cmp_gt_f32_e32 vcc, s0, v192
	v_pk_mul_f32 v[2:3], v[46:47], v[2:3]
	v_pk_mul_f32 v[84:85], v[84:85], v[130:131] op_sel_hi:[1,0]
	v_pk_fma_f32 v[106:107], v[196:197], v[2:3], v[58:59]
	v_pk_mul_f32 v[2:3], v[4:5], v[130:131] op_sel_hi:[1,0]
	v_mul_f32_e32 v4, 0x4b800000, v192
	v_pk_mul_f32 v[2:3], v[48:49], v[2:3]
	v_cndmask_b32_e32 v4, v192, v4, vcc
	v_pk_fma_f32 v[108:109], v[194:195], v[2:3], v[60:61]
	v_pk_mul_f32 v[2:3], v[6:7], v[130:131] op_sel_hi:[1,0]
	v_pk_mul_f32 v[82:83], v[82:83], v[130:131] op_sel_hi:[1,0]
	v_pk_mul_f32 v[84:85], v[36:37], v[84:85]
	v_pk_mul_f32 v[90:91], v[90:91], v[130:131] op_sel_hi:[1,0]
	v_pk_mul_f32 v[82:83], v[34:35], v[82:83]
	v_pk_fma_f32 v[84:85], v[144:145], v[84:85], v[28:29]
	v_pk_mul_f32 v[86:87], v[86:87], v[130:131] op_sel_hi:[1,0]
	v_pk_mul_f32 v[88:89], v[88:89], v[130:131] op_sel_hi:[1,0]
	v_pk_mul_f32 v[90:91], v[70:71], v[90:91]
	v_pk_fma_f32 v[82:83], v[146:147], v[82:83], v[26:27]
	v_pk_mul_f32 v[86:87], v[30:31], v[86:87]
	v_pk_mul_f32 v[88:89], v[32:33], v[88:89]
	v_pk_fma_f32 v[90:91], v[126:127], v[90:91], v[42:43]
	s_waitcnt vmcnt(5)
	v_pk_mul_f32 v[2:3], v[172:173], v[2:3]
	v_pk_fma_f32 v[86:87], v[188:189], v[86:87], v[50:51]
	s_waitcnt vmcnt(4)
	v_pk_fma_f32 v[110:111], v[114:115], v[2:3], v[176:177]
	v_pk_mul_f32 v[2:3], v[8:9], v[130:131] op_sel_hi:[1,0]
	v_pk_fma_f32 v[88:89], v[190:191], v[88:89], v[52:53]
	v_pk_mul_f32 v[2:3], v[174:175], v[2:3]
	v_pk_mul_f32 v[92:93], v[92:93], v[130:131] op_sel_hi:[1,0]
	v_pk_fma_f32 v[112:113], v[116:117], v[2:3], v[178:179]
	v_pk_mul_f32 v[2:3], v[14:15], v[130:131] op_sel_hi:[1,0]
	v_pk_mul_f32 v[92:93], v[72:73], v[92:93]
	s_waitcnt vmcnt(3)
	v_pk_mul_f32 v[2:3], v[168:169], v[2:3]
	v_pk_fma_f32 v[92:93], v[128:129], v[92:93], v[44:45]
	s_waitcnt vmcnt(2)
	v_pk_fma_f32 v[6:7], v[122:123], v[2:3], v[180:181]
	v_pk_mul_f32 v[2:3], v[16:17], v[130:131] op_sel_hi:[1,0]
	v_pk_mul_f32 v[94:95], v[94:95], v[130:131] op_sel_hi:[1,0]
	v_pk_mul_f32 v[2:3], v[170:171], v[2:3]
	v_pk_mul_f32 v[96:97], v[96:97], v[130:131] op_sel_hi:[1,0]
	v_pk_fma_f32 v[8:9], v[124:125], v[2:3], v[182:183]
	v_pk_mul_f32 v[2:3], v[10:11], v[130:131] op_sel_hi:[1,0]
	v_rsq_f32_e32 v10, v4
	v_pk_mul_f32 v[4:5], v[12:13], v[130:131] op_sel_hi:[1,0]
	v_pk_mul_f32 v[94:95], v[54:55], v[94:95]
	v_pk_mul_f32 v[96:97], v[56:57], v[96:97]
	v_mul_f32_e32 v11, 0x45800000, v10
	v_cndmask_b32_e32 v10, v10, v11, vcc
	v_pk_mul_f32 v[14:15], v[40:41], v[10:11] op_sel_hi:[1,0]
	v_pk_mul_f32 v[12:13], v[38:39], v[10:11] op_sel_hi:[1,0]
	v_pk_mul_f32 v[40:41], v[74:75], v[10:11] op_sel_hi:[1,0]
	v_pk_mul_f32 v[14:15], v[36:37], v[14:15]
	v_pk_mul_f32 v[12:13], v[34:35], v[12:13]
	v_pk_fma_f32 v[14:15], v[144:145], v[14:15], v[28:29]
	v_pk_mul_f32 v[28:29], v[70:71], v[40:41]
	v_pk_mul_f32 v[16:17], v[66:67], v[10:11] op_sel_hi:[1,0]
	v_pk_mul_f32 v[38:39], v[68:69], v[10:11] op_sel_hi:[1,0]
	v_pk_fma_f32 v[12:13], v[146:147], v[12:13], v[26:27]
	v_pk_fma_f32 v[28:29], v[126:127], v[28:29], v[42:43]
	v_cvt_pk_bf16_f32 v42, v82, v83
	v_cvt_pk_bf16_f32 v43, v84, v85
	v_pk_mul_f32 v[16:17], v[30:31], v[16:17]
	v_pk_mul_f32 v[26:27], v[32:33], v[38:39]
	global_store_dwordx2 v[136:137], v[42:43], off
	v_cvt_pk_bf16_f32 v42, v12, v13
	v_cvt_pk_bf16_f32 v43, v14, v15
	global_store_dwordx2 v[134:135], v[42:43], off
	ds_write_b128 v167, v[82:85]
	ds_write2_b64 v202, v[12:13], v[14:15] offset1:1
	v_cvt_pk_bf16_f32 v12, v86, v87
	v_cvt_pk_bf16_f32 v13, v88, v89
	v_pk_mul_f32 v[66:67], v[76:77], v[10:11] op_sel_hi:[1,0]
	v_pk_fma_f32 v[16:17], v[188:189], v[16:17], v[50:51]
	v_pk_fma_f32 v[26:27], v[190:191], v[26:27], v[52:53]
	global_store_dwordx2 v[136:137], v[12:13], off offset:512
	v_cvt_pk_bf16_f32 v12, v16, v17
	v_cvt_pk_bf16_f32 v13, v26, v27
	v_pk_mul_f32 v[30:31], v[72:73], v[66:67]
	global_store_dwordx2 v[134:135], v[12:13], off offset:512
	ds_write_b128 v167, v[86:89] offset:1024
	ds_write2_b64 v138, v[16:17], v[26:27] offset1:1
	v_cvt_pk_bf16_f32 v12, v90, v91
	v_cvt_pk_bf16_f32 v13, v92, v93
	v_pk_mul_f32 v[68:69], v[78:79], v[10:11] op_sel_hi:[1,0]
	v_pk_mul_f32 v[74:75], v[80:81], v[10:11] op_sel_hi:[1,0]
	v_pk_fma_f32 v[30:31], v[128:129], v[30:31], v[44:45]
	global_store_dwordx2 v[136:137], v[12:13], off offset:1024
	v_cvt_pk_bf16_f32 v12, v28, v29
	v_cvt_pk_bf16_f32 v13, v30, v31
	v_pk_fma_f32 v[94:95], v[118:119], v[94:95], v[62:63]
	v_pk_fma_f32 v[96:97], v[120:121], v[96:97], v[64:65]
	v_pk_mul_f32 v[32:33], v[54:55], v[68:69]
	v_pk_mul_f32 v[34:35], v[56:57], v[74:75]
	global_store_dwordx2 v[134:135], v[12:13], off offset:1024
	ds_write_b128 v167, v[90:93] offset:2048
	ds_write2_b64 v203, v[28:29], v[30:31] offset1:1
	v_cvt_pk_bf16_f32 v12, v94, v95
	v_cvt_pk_bf16_f32 v13, v96, v97
	v_pk_mul_f32 v[22:23], v[22:23], v[10:11] op_sel_hi:[1,0]
	v_pk_mul_f32 v[24:25], v[24:25], v[10:11] op_sel_hi:[1,0]
	v_pk_fma_f32 v[32:33], v[118:119], v[32:33], v[62:63]
	v_pk_fma_f32 v[34:35], v[120:121], v[34:35], v[64:65]
	global_store_dwordx2 v[136:137], v[12:13], off offset:1536
	v_cvt_pk_bf16_f32 v12, v32, v33
	v_cvt_pk_bf16_f32 v13, v34, v35
	v_pk_mul_f32 v[22:23], v[46:47], v[22:23]
	v_pk_mul_f32 v[24:25], v[48:49], v[24:25]
	global_store_dwordx2 v[134:135], v[12:13], off offset:1536
	ds_write_b128 v167, v[94:97] offset:3072
	ds_write2_b64 v204, v[32:33], v[34:35] offset1:1
	v_cvt_pk_bf16_f32 v12, v106, v107
	v_cvt_pk_bf16_f32 v13, v108, v109
	v_pk_mul_f32 v[18:19], v[18:19], v[10:11] op_sel_hi:[1,0]
	v_pk_mul_f32 v[20:21], v[20:21], v[10:11] op_sel_hi:[1,0]
	v_pk_fma_f32 v[22:23], v[196:197], v[22:23], v[58:59]
	v_pk_fma_f32 v[24:25], v[194:195], v[24:25], v[60:61]
	global_store_dwordx2 v[136:137], v[12:13], off offset:2048
	v_cvt_pk_bf16_f32 v12, v22, v23
	v_cvt_pk_bf16_f32 v13, v24, v25
	v_pk_mul_f32 v[18:19], v[172:173], v[18:19]
	v_pk_mul_f32 v[20:21], v[174:175], v[20:21]
	global_store_dwordx2 v[134:135], v[12:13], off offset:2048
	ds_write_b128 v167, v[106:109] offset:4096
	ds_write2_b64 v205, v[22:23], v[24:25] offset1:1
	v_cvt_pk_bf16_f32 v12, v110, v111
	v_cvt_pk_bf16_f32 v13, v112, v113
	v_pk_mul_f32 v[76:77], v[98:99], v[10:11] op_sel_hi:[1,0]
	v_pk_mul_f32 v[78:79], v[100:101], v[10:11] op_sel_hi:[1,0]
	v_pk_fma_f32 v[18:19], v[114:115], v[18:19], v[176:177]
	v_pk_fma_f32 v[20:21], v[116:117], v[20:21], v[178:179]
	global_store_dwordx2 v[136:137], v[12:13], off offset:2560
	v_cvt_pk_bf16_f32 v12, v18, v19
	v_cvt_pk_bf16_f32 v13, v20, v21
	s_waitcnt vmcnt(12)
; #define LAS __attribute__((address_space(3)))
; __device__ __forceinline__ unsigned cvt_pk_bf16(float lo, float hi) { unsigned r; asm volatile("v_cvt_pk_bf16_f32 %0, %1, %2" : "=v"(r) : "v"(lo), "v"(hi)); return r; }
; template <int NT>
; __device__ __forceinline__ void rows16_matmul(const LAS float* hfs, const float* W, int ldw, int col0, int wave, int lane, f32x4 (&acc)[NT]) {
; #pragma unroll
;     for (int jt = 0; jt < NT; ++jt) acc[jt] = (f32x4){0.f, 0.f, 0.f, 0.f};
;     const LAS float* ap = hfs + (lane & 15) * HFS_LD + wave * 256 + (lane >> 4);
;     const float* bp = W + (size_t)(wave * 256 + (lane >> 4)) * ldw + col0 + (lane & 15);
; __device__ __forceinline__ void route_phase(LAS unsigned char* lds, int bid, int G, const float* x, const float* g, const float* sc, const float* sh,
;                                             const float* rw, const float* rbias, bf16_t* hbuf, int* cnt, int* list, u32x2* rec) {
;     ...
;             for (int i = 0; i < 8; ++i) { const int c = (lane + 64 * i) * 4;
;                 u32x2 w; w.x = cvt_pk_bf16(va[i].x, va[i].y); w.y = cvt_pk_bf16(va[i].z, va[i].w); *(u32x2*)(hbuf + (size_t)row * D + c) = w;
;                 u32x2 w2; w2.x = cvt_pk_bf16(vb[i].x, vb[i].y); w2.y = cvt_pk_bf16(vb[i].z, vb[i].w); *(u32x2*)(hbuf + (size_t)(row + 1) * D + c) = w2;
;                 LAS float* hp = hfs + (wave * 2) * HFS_LD + c; hp[0] = va[i].x; hp[1] = va[i].y; hp[2] = va[i].z; hp[3] = va[i].w;
;                 hp[HFS_LD] = vb[i].x; hp[HFS_LD + 1] = vb[i].y; hp[HFS_LD + 2] = vb[i].z; hp[HFS_LD + 3] = vb[i].w; }
;         }
;         __syncthreads();
;         f32x4 acc[4];
;         rows16_matmul<4>(hfs, rw, NE, 0, wave, lane, acc);
	v_pk_mul_f32 v[2:3], v[184:185], v[2:3]
	v_pk_mul_f32 v[4:5], v[186:187], v[4:5]
	v_pk_mul_f32 v[80:81], v[102:103], v[10:11] op_sel_hi:[1,0]
	v_pk_mul_f32 v[10:11], v[104:105], v[10:11] op_sel_hi:[1,0]
	v_pk_mul_f32 v[36:37], v[168:169], v[76:77]
	v_pk_mul_f32 v[38:39], v[170:171], v[78:79]
	global_store_dwordx2 v[134:135], v[12:13], off offset:2560
	ds_write_b128 v167, v[110:113] offset:5120
	ds_write2_b64 v206, v[18:19], v[20:21] offset1:1
	v_cvt_pk_bf16_f32 v12, v6, v7
	v_cvt_pk_bf16_f32 v13, v8, v9
	s_waitcnt vmcnt(12)
	v_pk_fma_f32 v[2:3], v[198:199], v[2:3], v[140:141]
	v_pk_fma_f32 v[4:5], v[200:201], v[4:5], v[142:143]
	v_pk_fma_f32 v[36:37], v[122:123], v[36:37], v[180:181]
	v_pk_fma_f32 v[38:39], v[124:125], v[38:39], v[182:183]
	v_pk_mul_f32 v[40:41], v[184:185], v[80:81]
	v_pk_mul_f32 v[10:11], v[186:187], v[10:11]
	global_store_dwordx2 v[136:137], v[12:13], off offset:3072
	v_cvt_pk_bf16_f32 v12, v36, v37
	v_cvt_pk_bf16_f32 v13, v38, v39
	global_store_dwordx2 v[134:135], v[12:13], off offset:3072
	ds_write_b128 v167, v[6:9] offset:6144
	ds_write2_b64 v207, v[36:37], v[38:39] offset1:1
	v_cvt_pk_bf16_f32 v6, v2, v3
	v_cvt_pk_bf16_f32 v7, v4, v5
	v_pk_fma_f32 v[40:41], v[198:199], v[40:41], v[140:141]
	v_pk_fma_f32 v[10:11], v[200:201], v[10:11], v[142:143]
	global_store_dwordx2 v[136:137], v[6:7], off offset:3584
	v_cvt_pk_bf16_f32 v6, v40, v41
	v_cvt_pk_bf16_f32 v7, v10, v11
	global_store_dwordx2 v[134:135], v[6:7], off offset:3584
	ds_write_b128 v167, v[2:5] offset:7168
	ds_write2_b64 v193, v[40:41], v[10:11] offset1:1
	v_and_b32_e32 v4, 15, v1
	s_movk_i32 s0, 0x2008
	v_bfe_u32 v5, v1, 4, 2
	v_mad_u32_u24 v2, v4, s0, 0
	v_lshlrev_b32_e32 v3, 10, v166
	v_lshlrev_b32_e32 v6, 2, v5
	v_add3_u32 v20, v2, v3, v6
	v_lshl_or_b32 v2, v166, 8, v5
	v_ashrrev_i32_e32 v3, 31, v2
	v_lshlrev_b64 v[2:3], 8, v[2:3]
	v_lshl_add_u64 v[2:3], s[4:5], 0, v[2:3]
	v_lshlrev_b32_e32 v130, 2, v4
	v_lshl_add_u64 v[18:19], v[2:3], 0, v[130:131]
	s_mov_b64 s[0:1], 0
	v_mov_b32_e32 v2, 0
	v_mov_b32_e32 v3, v131
	v_mov_b32_e32 v4, v131
	v_mov_b32_e32 v5, v131
	v_mov_b32_e32 v6, 0
	v_mov_b32_e32 v7, v131
	v_mov_b32_e32 v8, v131
	v_mov_b32_e32 v9, v131
	v_mov_b32_e32 v10, 0
	v_mov_b32_e32 v11, v131
	v_mov_b32_e32 v12, v131
	v_mov_b32_e32 v13, v131
	v_mov_b32_e32 v14, 0
	v_mov_b32_e32 v15, v131
	v_mov_b32_e32 v16, v131
	v_mov_b32_e32 v17, v131
	s_waitcnt lgkmcnt(0)
	s_barrier

; __device__ __forceinline__ void row_norm_mod2(float4 (&v0)[8], float4 (&v1)[8], int lane, const float* g, const float* sc, const float* sh) {
;     float4 ga[8], s1a[8];
; #pragma unroll
;     for (int i = 0; i < 8; ++i) { const int c = (lane + 64 * i) * 4; ga[i] = *(const float4*)(g + c); s1a[i] = *(const float4*)(sc + c); }
;     float ssa = 0.f, ssb = 0.f;
; #pragma unroll
;     for (int i = 0; i < 8; ++i) { ssa += v0[i].x * v0[i].x + v0[i].y * v0[i].y + v0[i].z * v0[i].z + v0[i].w * v0[i].w; ssb += v1[i].x * v1[i].x + v1[i].y * v1[i].y + v1[i].z * v1[i].z + v1[i].w * v1[i].w; }
; __device__ __forceinline__ void route_phase(LAS unsigned char* lds, int bid, int G, const float* x, const float* g, const float* sc, const float* sh,
;                                             const float* rw, const float* rbias, bf16_t* hbuf, int* cnt, int* list, u32x2* rec) {
;     ...
;         {   const int row = r0 + wave * 2;
;             float4 va[8], vb[8];
; #pragma unroll
;             for (int i = 0; i < 8; ++i) { va[i] = *(const float4*)(x + (size_t)row * D + (lane + 64 * i) * 4); vb[i] = *(const float4*)(x + (size_t)(row + 1) * D + (lane + 64 * i) * 4); }
;             row_norm_mod2(va, vb, lane, g, sc, sh);
.LBB0_1740:
	v_mov_b32_e32 v1, v0
	v_mov_b32_e32 v47, v143
	v_ashrrev_i32_e32 v172, 6, v1
	v_lshlrev_b32_e32 v168, 1, v172
	v_add_u32_e32 v30, s33, v168
	v_and_b32_e32 v167, 63, v1
	v_ashrrev_i32_e32 v31, 31, v30
	v_lshlrev_b64 v[2:3], 13, v[30:31]
	v_lshlrev_b32_e32 v142, 4, v167
	v_lshl_add_u64 v[10:11], s[68:69], 0, v[2:3]
	v_or_b32_e32 v46, 0x1000, v142
	v_or_b32_e32 v150, 0x1400, v142
	v_mov_b32_e32 v151, v143
	v_lshl_add_u64 v[2:3], v[10:11], 0, v[46:47]
	v_lshl_add_u64 v[6:7], v[10:11], 0, v[150:151]
	s_barrier
	global_load_dwordx4 v[2:5], v[2:3], off nt
	v_or_b32_e32 v32, 1, v30
	global_load_dwordx4 v[6:9], v[6:7], off nt
	v_ashrrev_i32_e32 v33, 31, v32
	v_or_b32_e32 v154, 0x1800, v142
	v_mov_b32_e32 v155, v143
	v_lshlrev_b64 v[12:13], 13, v[32:33]
	v_lshl_add_u64 v[20:21], v[10:11], 0, v[154:155]
	v_or_b32_e32 v152, 0x1c00, v142
	v_mov_b32_e32 v153, v143
	v_lshl_add_u64 v[18:19], s[68:69], 0, v[12:13]
	v_lshl_add_u64 v[48:49], v[10:11], 0, v[142:143]
	s_waitcnt lgkmcnt(0)
	v_lshl_add_u64 v[22:23], v[10:11], 0, v[152:153]
	global_load_dwordx4 v[14:17], v[20:21], off nt
	global_load_dwordx4 v[10:13], v[22:23], off nt
	v_cmp_lt_i32_e32 vcc, v158, v157
	v_lshl_add_u64 v[78:79], v[18:19], 0, v[142:143]
	v_lshl_add_u64 v[26:27], v[18:19], 0, v[46:47]
	v_lshl_add_u64 v[28:29], v[18:19], 0, v[150:151]
	v_lshl_add_u64 v[110:111], v[18:19], 0, v[154:155]
	v_lshl_add_u64 v[114:115], v[18:19], 0, v[152:153]
	v_cndmask_b32_e32 v18, v145, v158, vcc
	v_cmp_lt_i32_e32 vcc, v159, v157
	v_lshlrev_b32_e32 v151, 2, v18
	global_load_dwordx4 v[18:21], v[26:27], off nt
	global_load_dwordx4 v[22:25], v[28:29], off nt
	v_cndmask_b32_e32 v34, v145, v159, vcc
	v_cmp_lt_i32_e32 vcc, v160, v157
	v_readlane_b32 s0, v254, 33
	v_lshlrev_b64 v[30:31], 12, v[30:31]
	v_cndmask_b32_e32 v26, v145, v160, vcc
	v_cmp_lt_i32_e32 vcc, v161, v157
	v_lshlrev_b32_e32 v155, 2, v26
	v_readlane_b32 s1, v254, 34
	v_cndmask_b32_e32 v26, v145, v161, vcc
	v_cmp_lt_i32_e32 vcc, v162, v157
	v_lshlrev_b32_e32 v169, 2, v26
	v_lshlrev_b64 v[32:33], 12, v[32:33]
	v_cndmask_b32_e32 v26, v145, v162, vcc
	v_lshlrev_b32_e32 v170, 2, v26
	global_load_dwordx4 v[26:29], v[78:79], off nt
	global_load_dwordx4 v[94:97], v[48:49], off nt
	global_load_dwordx4 v[74:77], v[78:79], off offset:1024 nt
	global_load_dwordx4 v[98:101], v[48:49], off offset:1024 nt
	v_cmp_lt_i32_e32 vcc, v163, v157
	v_lshl_add_u64 v[30:31], s[0:1], 0, v[30:31]
	v_lshl_add_u64 v[32:33], s[0:1], 0, v[32:33]
	s_movk_i32 s0, 0x4010
	v_lshlrev_b32_e32 v153, 2, v34
	v_cndmask_b32_e32 v34, v145, v163, vcc
	v_mul_lo_u32 v36, v172, s0
	v_readlane_b32 s0, v254, 42
	v_readlane_b32 s2, v254, 29
	v_readlane_b32 s4, v254, 31
	v_or_b32_e32 v47, 0x400, v142
	v_or_b32_e32 v54, 0x800, v142
	v_or_b32_e32 v55, 0xc00, v142
	v_lshlrev_b32_e32 v171, 2, v34
	v_lshlrev_b32_e32 v34, 3, v167
	v_mov_b32_e32 v35, v143
	v_readlane_b32 s1, v254, 43
	v_readlane_b32 s3, v254, 30
	v_readlane_b32 s5, v254, 32
	v_lshl_add_u64 v[148:149], v[30:31], 0, v[34:35]
	v_lshl_add_u64 v[146:147], v[32:33], 0, v[34:35]
	v_add3_u32 v173, 0, v36, v142
	global_load_dwordx4 v[30:33], v142, s[0:1] nt
	global_load_dwordx4 v[174:177], v142, s[2:3] nt
	global_load_dwordx4 v[50:53], v142, s[4:5] nt
	global_load_dwordx4 v[34:37], v47, s[0:1] nt
	global_load_dwordx4 v[178:181], v47, s[2:3] nt
	global_load_dwordx4 v[38:41], v47, s[4:5] nt
	global_load_dwordx4 v[102:105], v[48:49], off offset:2048 nt
	global_load_dwordx4 v[86:89], v[78:79], off offset:2048 nt
	global_load_dwordx4 v[42:45], v54, s[0:1] nt
	global_load_dwordx4 v[134:137], v54, s[2:3] nt
	global_load_dwordx4 v[66:69], v54, s[4:5] nt
	global_load_dwordx4 v[106:109], v[48:49], off offset:3072 nt
	global_load_dwordx4 v[58:61], v55, s[0:1] nt
	global_load_dwordx4 v[130:133], v55, s[2:3] nt
	global_load_dwordx4 v[70:73], v55, s[4:5] nt
	s_nop 0
	global_load_dwordx4 v[54:57], v46, s[0:1] nt
	global_load_dwordx4 v[122:125], v46, s[2:3] nt
	global_load_dwordx4 v[62:65], v46, s[4:5] nt
	s_nop 0
	global_load_dwordx4 v[46:49], v150, s[0:1] nt
	global_load_dwordx4 v[126:129], v150, s[2:3] nt
	global_load_dwordx4 v[90:93], v[78:79], off offset:3072 nt
	v_add_u32_e32 v204, 0x2c08, v173
	v_add_u32_e32 v205, 0x3008, v173
	v_add_u32_e32 v206, 0x3408, v173
	v_add_u32_e32 v207, 0x3808, v173
	s_waitcnt vmcnt(30)
	v_mov_b32_e32 v78, v3
	v_mov_b32_e32 v80, v2
	s_waitcnt vmcnt(29)
	v_mov_b32_e32 v79, v7
	v_mov_b32_e32 v81, v6
	v_pk_mul_f32 v[78:79], v[78:79], v[78:79]
	v_mov_b32_e32 v82, v5
	v_pk_fma_f32 v[78:79], v[80:81], v[80:81], v[78:79]
	v_mov_b32_e32 v80, v4
	v_mov_b32_e32 v81, v8
	v_mov_b32_e32 v83, v9
	v_pk_fma_f32 v[78:79], v[80:81], v[80:81], v[78:79]
	s_waitcnt vmcnt(28)
	v_mov_b32_e32 v186, v15
	v_pk_fma_f32 v[182:183], v[82:83], v[82:83], v[78:79]
	global_load_dwordx4 v[82:85], v154, s[0:1] nt
	global_load_dwordx4 v[138:141], v154, s[2:3] nt
	global_load_dwordx4 v[78:81], v152, s[0:1] nt
	global_load_dwordx4 v[118:121], v152, s[2:3] nt
	s_nop 0
	global_load_dwordx4 v[110:113], v[110:111], off nt
	s_nop 0
	global_load_dwordx4 v[114:117], v[114:115], off nt
	s_waitcnt vmcnt(33)
	v_mov_b32_e32 v187, v11
	v_mov_b32_e32 v184, v14
	v_mov_b32_e32 v185, v10
	v_pk_mul_f32 v[186:187], v[186:187], v[186:187]
	v_mov_b32_e32 v188, v17
	v_pk_fma_f32 v[184:185], v[184:185], v[184:185], v[186:187]
	v_mov_b32_e32 v186, v16
	v_mov_b32_e32 v187, v12
	v_mov_b32_e32 v189, v13
	v_pk_fma_f32 v[184:185], v[186:187], v[186:187], v[184:185]
	s_waitcnt vmcnt(32)
	v_mov_b32_e32 v186, v18
	v_pk_fma_f32 v[184:185], v[188:189], v[188:189], v[184:185]
	v_mov_b32_e32 v188, v19
	s_waitcnt vmcnt(31)
; __device__ __forceinline__ void row_norm_mod2(float4 (&v0)[8], float4 (&v1)[8], int lane, const float* g, const float* sc, const float* sh) {
;     ...
;     float ssa = 0.f, ssb = 0.f;
; #pragma unroll
;     for (int i = 0; i < 8; ++i) { ssa += v0[i].x * v0[i].x + v0[i].y * v0[i].y + v0[i].z * v0[i].z + v0[i].w * v0[i].w; ssb += v1[i].x * v1[i].x + v1[i].y * v1[i].y + v1[i].z * v1[i].z + v1[i].w * v1[i].w; }
;     ssa = wave_sum(ssa); ssb = wave_sum(ssb);
;     const float ra = rsqrtf(ssa * (1.f / D) + EPS), rb = rsqrtf(ssb * (1.f / D) + EPS);
; #pragma unroll
;     for (int i = 0; i < 8; ++i) { const int c = (lane + 64 * i) * 4; const float4 gg = ga[i], s1 = s1a[i], s0 = *(const float4*)(sh + c);
	v_mov_b32_e32 v189, v23
	v_mov_b32_e32 v187, v22
	v_pk_mul_f32 v[188:189], v[188:189], v[188:189]
	v_mov_b32_e32 v190, v21
	v_pk_fma_f32 v[186:187], v[186:187], v[186:187], v[188:189]
	v_mov_b32_e32 v188, v20
	v_mov_b32_e32 v189, v24
	v_mov_b32_e32 v191, v25
	v_pk_fma_f32 v[186:187], v[188:189], v[188:189], v[186:187]
	s_waitcnt vmcnt(30)
	v_mov_b32_e32 v188, v26
	v_pk_fma_f32 v[186:187], v[190:191], v[190:191], v[186:187]
	v_mov_b32_e32 v190, v27
	s_waitcnt vmcnt(29)
	v_mov_b32_e32 v191, v95
	v_mov_b32_e32 v189, v94
	v_pk_mul_f32 v[190:191], v[190:191], v[190:191]
	v_mov_b32_e32 v192, v29
	v_pk_fma_f32 v[188:189], v[188:189], v[188:189], v[190:191]
	v_mov_b32_e32 v190, v28
	v_mov_b32_e32 v191, v96
	v_mov_b32_e32 v193, v97
	v_pk_fma_f32 v[188:189], v[190:191], v[190:191], v[188:189]
	s_waitcnt vmcnt(28)
	v_mov_b32_e32 v190, v74
	v_pk_fma_f32 v[188:189], v[192:193], v[192:193], v[188:189]
	v_mov_b32_e32 v192, v75
	s_waitcnt vmcnt(27)
	v_mov_b32_e32 v193, v99
	v_mov_b32_e32 v191, v98
	v_pk_mul_f32 v[192:193], v[192:193], v[192:193]
	v_mov_b32_e32 v194, v77
	v_pk_fma_f32 v[190:191], v[190:191], v[190:191], v[192:193]
	v_mov_b32_e32 v192, v76
	v_mov_b32_e32 v193, v100
	v_mov_b32_e32 v195, v101
	v_pk_fma_f32 v[190:191], v[192:193], v[192:193], v[190:191]
	s_waitcnt vmcnt(19)
	v_mov_b32_e32 v192, v87
	v_pk_fma_f32 v[190:191], v[194:195], v[194:195], v[190:191]
	v_mov_b32_e32 v193, v103
	v_pk_add_f32 v[188:189], v[188:189], v[190:191]
	v_mov_b32_e32 v190, v86
	v_mov_b32_e32 v191, v102
	v_pk_mul_f32 v[192:193], v[192:193], v[192:193]
	v_mov_b32_e32 v194, v89
	v_pk_fma_f32 v[190:191], v[190:191], v[190:191], v[192:193]
	v_mov_b32_e32 v192, v88
	v_mov_b32_e32 v193, v104
	v_mov_b32_e32 v195, v105
	v_pk_fma_f32 v[190:191], v[192:193], v[192:193], v[190:191]
	s_waitcnt vmcnt(6)
	v_mov_b32_e32 v192, v91
	v_pk_fma_f32 v[190:191], v[194:195], v[194:195], v[190:191]
	v_mov_b32_e32 v193, v107
	v_pk_add_f32 v[188:189], v[188:189], v[190:191]
	v_mov_b32_e32 v190, v90
	v_mov_b32_e32 v191, v106
	v_pk_mul_f32 v[192:193], v[192:193], v[192:193]
	v_mov_b32_e32 v194, v93
	v_pk_fma_f32 v[190:191], v[190:191], v[190:191], v[192:193]
	v_mov_b32_e32 v192, v92
	v_mov_b32_e32 v193, v108
	v_mov_b32_e32 v195, v109
	v_pk_fma_f32 v[190:191], v[192:193], v[192:193], v[190:191]
	v_pk_add_f32 v[196:197], v[180:181], 1.0 op_sel_hi:[1,0]
	v_pk_fma_f32 v[190:191], v[194:195], v[194:195], v[190:191]
	v_pk_add_f32 v[198:199], v[122:123], 1.0 op_sel_hi:[1,0]
	v_pk_add_f32 v[188:189], v[188:189], v[190:191]
	v_mov_b32_e32 v190, v186
	v_mov_b32_e32 v191, v182
	s_waitcnt vmcnt(1)
	v_mov_b32_e32 v192, v111
	s_waitcnt vmcnt(0)
	v_mov_b32_e32 v193, v115
	v_pk_add_f32 v[188:189], v[188:189], v[190:191]
	v_mov_b32_e32 v190, v110
	v_mov_b32_e32 v191, v114
	v_pk_mul_f32 v[192:193], v[192:193], v[192:193]
	v_mov_b32_e32 v194, v113
	v_pk_fma_f32 v[190:191], v[190:191], v[190:191], v[192:193]
	v_mov_b32_e32 v192, v112
	v_mov_b32_e32 v193, v116
	v_mov_b32_e32 v195, v117
	v_pk_fma_f32 v[190:191], v[192:193], v[192:193], v[190:191]
	v_mov_b32_e32 v182, v187
	v_pk_fma_f32 v[190:191], v[194:195], v[194:195], v[190:191]
	v_pk_add_f32 v[182:183], v[188:189], v[182:183]
	v_mov_b32_e32 v186, v190
	v_mov_b32_e32 v187, v184
	v_pk_add_f32 v[182:183], v[182:183], v[186:187]
	v_mov_b32_e32 v184, v191
	v_pk_add_f32 v[182:183], v[182:183], v[184:185]
	ds_bpermute_b32 v185, v151, v183
	ds_bpermute_b32 v184, v151, v182
	v_pk_add_f32 v[186:187], v[174:175], 1.0 op_sel_hi:[1,0]
	v_pk_add_f32 v[188:189], v[176:177], 1.0 op_sel_hi:[1,0]
	global_load_dwordx4 v[174:177], v150, s[4:5] nt
	v_pk_add_f32 v[194:195], v[178:179], 1.0 op_sel_hi:[1,0]
	s_waitcnt lgkmcnt(0)
	v_pk_add_f32 v[190:191], v[182:183], v[184:185]
	global_load_dwordx4 v[182:185], v154, s[4:5] nt
	global_load_dwordx4 v[178:181], v152, s[4:5] nt
	ds_bpermute_b32 v193, v153, v191
	ds_bpermute_b32 v192, v153, v190
	s_mov_b32 s0, 0x3a000000
	v_pk_add_f32 v[200:201], v[118:119], 1.0 op_sel_hi:[1,0]
	v_pk_add_f32 v[202:203], v[120:121], 1.0 op_sel_hi:[1,0]
	v_pk_add_f32 v[126:127], v[126:127], 1.0 op_sel_hi:[1,0]
	s_waitcnt lgkmcnt(0)
	v_pk_add_f32 v[190:191], v[190:191], v[192:193]
	ds_bpermute_b32 v193, v155, v191
	ds_bpermute_b32 v192, v155, v190
	v_pk_add_f32 v[128:129], v[128:129], 1.0 op_sel_hi:[1,0]
	v_pk_add_f32 v[138:139], v[138:139], 1.0 op_sel_hi:[1,0]
	v_pk_add_f32 v[140:141], v[140:141], 1.0 op_sel_hi:[1,0]
	v_add_u32_e32 v150, 0x2008, v173
	s_waitcnt lgkmcnt(0)
	v_pk_add_f32 v[190:191], v[190:191], v[192:193]
	ds_bpermute_b32 v193, v169, v191
	ds_bpermute_b32 v192, v169, v190
	v_pk_add_f32 v[134:135], v[134:135], 1.0 op_sel_hi:[1,0]
	v_pk_add_f32 v[136:137], v[136:137], 1.0 op_sel_hi:[1,0]
	v_add_u32_e32 v154, 0x2408, v173
	v_pk_add_f32 v[130:131], v[130:131], 1.0 op_sel_hi:[1,0]
	s_waitcnt lgkmcnt(0)
	v_pk_add_f32 v[122:123], v[190:191], v[192:193]
	ds_bpermute_b32 v191, v170, v123
	ds_bpermute_b32 v190, v170, v122
	v_pk_add_f32 v[192:193], v[124:125], 1.0 op_sel_hi:[1,0]
	v_pk_add_f32 v[132:133], v[132:133], 1.0 op_sel_hi:[1,0]
	v_add_u32_e32 v152, 0x2808, v173
	s_waitcnt lgkmcnt(0)
	v_pk_add_f32 v[122:123], v[122:123], v[190:191]
	ds_bpermute_b32 v125, v171, v123
	ds_bpermute_b32 v124, v171, v122
	s_waitcnt lgkmcnt(0)
; __device__ __forceinline__ void row_norm_mod2(float4 (&v0)[8], float4 (&v1)[8], int lane, const float* g, const float* sc, const float* sh) {
;     ...
;     const float ra = rsqrtf(ssa * (1.f / D) + EPS), rb = rsqrtf(ssb * (1.f / D) + EPS);
; #pragma unroll
;     for (int i = 0; i < 8; ++i) { const int c = (lane + 64 * i) * 4; const float4 gg = ga[i], s1 = s1a[i], s0 = *(const float4*)(sh + c);
;         v0[i].x = v0[i].x * ra * gg.x * (1.f + s1.x) + s0.x; v0[i].y = v0[i].y * ra * gg.y * (1.f + s1.y) + s0.y; v0[i].z = v0[i].z * ra * gg.z * (1.f + s1.z) + s0.z; v0[i].w = v0[i].w * ra * gg.w * (1.f + s1.w) + s0.w;
;         v1[i].x = v1[i].x * rb * gg.x * (1.f + s1.x) + s0.x; v1[i].y = v1[i].y * rb * gg.y * (1.f + s1.y) + s0.y; v1[i].z = v1[i].z * rb * gg.z * (1.f + s1.z) + s0.z; v1[i].w = v1[i].w * rb * gg.w * (1.f + s1.w) + s0.w; }
	v_pk_add_f32 v[122:123], v[122:123], v[124:125]
	s_nop 0
	v_pk_fma_f32 v[190:191], v[122:123], s[0:1], v[144:145] op_sel_hi:[1,0,0]
	s_mov_b32 s0, 0x800000
	v_mul_f32_e32 v122, 0x4b800000, v191
	v_cmp_gt_f32_e32 vcc, s0, v191
	s_nop 1
	v_cndmask_b32_e32 v122, v191, v122, vcc
	v_rsq_f32_e32 v122, v122
	v_add_u32_e32 v191, 0x3c08, v173
	v_mul_f32_e32 v118, 0x45800000, v122
	v_cndmask_b32_e32 v142, v122, v118, vcc
	v_pk_mul_f32 v[2:3], v[2:3], v[142:143] op_sel_hi:[1,0]
	v_cmp_gt_f32_e32 vcc, s0, v190
	v_pk_mul_f32 v[2:3], v[54:55], v[2:3]
	v_pk_mul_f32 v[94:95], v[94:95], v[142:143] op_sel_hi:[1,0]
	v_pk_fma_f32 v[118:119], v[198:199], v[2:3], v[62:63]
	v_pk_mul_f32 v[2:3], v[4:5], v[142:143] op_sel_hi:[1,0]
	v_mul_f32_e32 v4, 0x4b800000, v190
	v_pk_mul_f32 v[2:3], v[56:57], v[2:3]
	v_cndmask_b32_e32 v4, v190, v4, vcc
	v_pk_fma_f32 v[120:121], v[192:193], v[2:3], v[64:65]
	v_pk_mul_f32 v[2:3], v[6:7], v[142:143] op_sel_hi:[1,0]
	v_pk_mul_f32 v[96:97], v[96:97], v[142:143] op_sel_hi:[1,0]
	v_pk_mul_f32 v[2:3], v[46:47], v[2:3]
	v_pk_mul_f32 v[94:95], v[30:31], v[94:95]
	v_pk_mul_f32 v[96:97], v[32:33], v[96:97]
	v_pk_mul_f32 v[98:99], v[98:99], v[142:143] op_sel_hi:[1,0]
	v_pk_mul_f32 v[100:101], v[100:101], v[142:143] op_sel_hi:[1,0]
	v_pk_mul_f32 v[102:103], v[102:103], v[142:143] op_sel_hi:[1,0]
	v_pk_fma_f32 v[94:95], v[186:187], v[94:95], v[50:51]
	v_pk_fma_f32 v[96:97], v[188:189], v[96:97], v[52:53]
	v_pk_mul_f32 v[98:99], v[34:35], v[98:99]
	v_pk_mul_f32 v[100:101], v[36:37], v[100:101]
	v_pk_mul_f32 v[102:103], v[42:43], v[102:103]
	v_pk_fma_f32 v[98:99], v[194:195], v[98:99], v[38:39]
	v_pk_fma_f32 v[100:101], v[196:197], v[100:101], v[40:41]
	v_pk_mul_f32 v[104:105], v[104:105], v[142:143] op_sel_hi:[1,0]
	v_pk_fma_f32 v[102:103], v[134:135], v[102:103], v[66:67]
	s_waitcnt vmcnt(2)
	v_pk_fma_f32 v[122:123], v[126:127], v[2:3], v[174:175]
	v_pk_mul_f32 v[2:3], v[8:9], v[142:143] op_sel_hi:[1,0]
	v_pk_mul_f32 v[104:105], v[44:45], v[104:105]
	v_pk_mul_f32 v[2:3], v[48:49], v[2:3]
	v_pk_fma_f32 v[104:105], v[136:137], v[104:105], v[68:69]
	v_pk_fma_f32 v[124:125], v[128:129], v[2:3], v[176:177]
	v_pk_mul_f32 v[2:3], v[14:15], v[142:143] op_sel_hi:[1,0]
	v_pk_mul_f32 v[106:107], v[106:107], v[142:143] op_sel_hi:[1,0]
	v_pk_mul_f32 v[2:3], v[82:83], v[2:3]
	v_pk_mul_f32 v[108:109], v[108:109], v[142:143] op_sel_hi:[1,0]
	s_waitcnt vmcnt(1)
; #define LAS __attribute__((address_space(3)))
; __device__ __forceinline__ void row_norm_mod2(float4 (&v0)[8], float4 (&v1)[8], int lane, const float* g, const float* sc, const float* sh) {
;     ...
;     const float ra = rsqrtf(ssa * (1.f / D) + EPS), rb = rsqrtf(ssb * (1.f / D) + EPS);
; #pragma unroll
;     for (int i = 0; i < 8; ++i) { const int c = (lane + 64 * i) * 4; const float4 gg = ga[i], s1 = s1a[i], s0 = *(const float4*)(sh + c);
;         v0[i].x = v0[i].x * ra * gg.x * (1.f + s1.x) + s0.x; v0[i].y = v0[i].y * ra * gg.y * (1.f + s1.y) + s0.y; v0[i].z = v0[i].z * ra * gg.z * (1.f + s1.z) + s0.z; v0[i].w = v0[i].w * ra * gg.w * (1.f + s1.w) + s0.w;
;         v1[i].x = v1[i].x * rb * gg.x * (1.f + s1.x) + s0.x; v1[i].y = v1[i].y * rb * gg.y * (1.f + s1.y) + s0.y; v1[i].z = v1[i].z * rb * gg.z * (1.f + s1.z) + s0.z; v1[i].w = v1[i].w * rb * gg.w * (1.f + s1.w) + s0.w; }
; }
; template <int NT>
; __device__ __forceinline__ void rows16_matmul(const LAS float* hfs, const float* W, int ldw, int col0, int wave, int lane, f32x4 (&acc)[NT]) {
; #pragma unroll
;     for (int jt = 0; jt < NT; ++jt) acc[jt] = (f32x4){0.f, 0.f, 0.f, 0.f};
;     const LAS float* ap = hfs + (lane & 15) * HFS_LD + wave * 256 + (lane >> 4);
;     const float* bp = W + (size_t)(wave * 256 + (lane >> 4)) * ldw + col0 + (lane & 15);
; __device__ __forceinline__ void route_phase(LAS unsigned char* lds, int bid, int G, const float* x, const float* g, const float* sc, const float* sh,
;                                             const float* rw, const float* rbias, bf16_t* hbuf, int* cnt, int* list, u32x2* rec) {
;     ...
;             for (int i = 0; i < 8; ++i) { const int c = (lane + 64 * i) * 4;
;                 u32x2 w; w.x = cvt_pk_bf16(va[i].x, va[i].y); w.y = cvt_pk_bf16(va[i].z, va[i].w); *(u32x2*)(hbuf + (size_t)row * D + c) = w;
;                 u32x2 w2; w2.x = cvt_pk_bf16(vb[i].x, vb[i].y); w2.y = cvt_pk_bf16(vb[i].z, vb[i].w); *(u32x2*)(hbuf + (size_t)(row + 1) * D + c) = w2;
;                 LAS float* hp = hfs + (wave * 2) * HFS_LD + c; hp[0] = va[i].x; hp[1] = va[i].y; hp[2] = va[i].z; hp[3] = va[i].w;
;                 hp[HFS_LD] = vb[i].x; hp[HFS_LD + 1] = vb[i].y; hp[HFS_LD + 2] = vb[i].z; hp[HFS_LD + 3] = vb[i].w; }
	v_pk_fma_f32 v[6:7], v[138:139], v[2:3], v[182:183]
	v_pk_mul_f32 v[2:3], v[16:17], v[142:143] op_sel_hi:[1,0]
	v_pk_mul_f32 v[106:107], v[58:59], v[106:107]
	v_pk_mul_f32 v[2:3], v[84:85], v[2:3]
	v_pk_mul_f32 v[108:109], v[60:61], v[108:109]
	v_pk_fma_f32 v[8:9], v[140:141], v[2:3], v[184:185]
	v_pk_mul_f32 v[2:3], v[10:11], v[142:143] op_sel_hi:[1,0]
	v_rsq_f32_e32 v10, v4
	v_pk_mul_f32 v[4:5], v[12:13], v[142:143] op_sel_hi:[1,0]
	v_pk_fma_f32 v[106:107], v[130:131], v[106:107], v[70:71]
	v_pk_fma_f32 v[108:109], v[132:133], v[108:109], v[72:73]
	v_mul_f32_e32 v11, 0x45800000, v10
	v_cndmask_b32_e32 v10, v10, v11, vcc
	v_pk_mul_f32 v[12:13], v[26:27], v[10:11] op_sel_hi:[1,0]
	v_pk_mul_f32 v[14:15], v[28:29], v[10:11] op_sel_hi:[1,0]
	v_pk_mul_f32 v[28:29], v[86:87], v[10:11] op_sel_hi:[1,0]
	v_pk_mul_f32 v[12:13], v[30:31], v[12:13]
	v_pk_mul_f32 v[16:17], v[74:75], v[10:11] op_sel_hi:[1,0]
	v_pk_mul_f32 v[26:27], v[76:77], v[10:11] op_sel_hi:[1,0]
	v_pk_fma_f32 v[12:13], v[186:187], v[12:13], v[50:51]
	v_pk_mul_f32 v[14:15], v[32:33], v[14:15]
	v_pk_mul_f32 v[28:29], v[42:43], v[28:29]
	v_cvt_pk_bf16_f32 v42, v94, v95
	v_cvt_pk_bf16_f32 v43, v96, v97
	v_pk_fma_f32 v[14:15], v[188:189], v[14:15], v[52:53]
	v_pk_mul_f32 v[16:17], v[34:35], v[16:17]
	v_pk_mul_f32 v[26:27], v[36:37], v[26:27]
	global_store_dwordx2 v[148:149], v[42:43], off
	v_cvt_pk_bf16_f32 v42, v12, v13
	v_cvt_pk_bf16_f32 v43, v14, v15
	global_store_dwordx2 v[146:147], v[42:43], off
	ds_write_b128 v173, v[94:97]
	ds_write2_b64 v150, v[12:13], v[14:15] offset1:1
	v_cvt_pk_bf16_f32 v12, v98, v99
	v_cvt_pk_bf16_f32 v13, v100, v101
	v_pk_mul_f32 v[74:75], v[88:89], v[10:11] op_sel_hi:[1,0]
	v_pk_fma_f32 v[16:17], v[194:195], v[16:17], v[38:39]
	v_pk_fma_f32 v[26:27], v[196:197], v[26:27], v[40:41]
	global_store_dwordx2 v[148:149], v[12:13], off offset:512
	v_cvt_pk_bf16_f32 v12, v16, v17
	v_cvt_pk_bf16_f32 v13, v26, v27
	v_pk_mul_f32 v[30:31], v[44:45], v[74:75]
	global_store_dwordx2 v[146:147], v[12:13], off offset:512
	ds_write_b128 v173, v[98:101] offset:1024
	ds_write2_b64 v154, v[16:17], v[26:27] offset1:1
	v_cvt_pk_bf16_f32 v12, v102, v103
	v_cvt_pk_bf16_f32 v13, v104, v105
	v_pk_mul_f32 v[76:77], v[90:91], v[10:11] op_sel_hi:[1,0]
	v_pk_mul_f32 v[86:87], v[92:93], v[10:11] op_sel_hi:[1,0]
	v_pk_fma_f32 v[28:29], v[134:135], v[28:29], v[66:67]
	v_pk_fma_f32 v[30:31], v[136:137], v[30:31], v[68:69]
	global_store_dwordx2 v[148:149], v[12:13], off offset:1024
	v_cvt_pk_bf16_f32 v12, v28, v29
	v_cvt_pk_bf16_f32 v13, v30, v31
	v_pk_mul_f32 v[32:33], v[58:59], v[76:77]
	v_pk_mul_f32 v[34:35], v[60:61], v[86:87]
	global_store_dwordx2 v[146:147], v[12:13], off offset:1024
	ds_write_b128 v173, v[102:105] offset:2048
	ds_write2_b64 v152, v[28:29], v[30:31] offset1:1
	v_cvt_pk_bf16_f32 v12, v106, v107
	v_cvt_pk_bf16_f32 v13, v108, v109
	v_pk_mul_f32 v[18:19], v[18:19], v[10:11] op_sel_hi:[1,0]
	v_pk_mul_f32 v[20:21], v[20:21], v[10:11] op_sel_hi:[1,0]
	v_pk_fma_f32 v[32:33], v[130:131], v[32:33], v[70:71]
	v_pk_fma_f32 v[34:35], v[132:133], v[34:35], v[72:73]
	global_store_dwordx2 v[148:149], v[12:13], off offset:1536
	v_cvt_pk_bf16_f32 v12, v32, v33
	v_cvt_pk_bf16_f32 v13, v34, v35
	v_pk_mul_f32 v[18:19], v[54:55], v[18:19]
	v_pk_mul_f32 v[20:21], v[56:57], v[20:21]
	global_store_dwordx2 v[146:147], v[12:13], off offset:1536
	ds_write_b128 v173, v[106:109] offset:3072
	ds_write2_b64 v204, v[32:33], v[34:35] offset1:1
	v_cvt_pk_bf16_f32 v12, v118, v119
	v_cvt_pk_bf16_f32 v13, v120, v121
	v_pk_mul_f32 v[22:23], v[22:23], v[10:11] op_sel_hi:[1,0]
	v_pk_mul_f32 v[24:25], v[24:25], v[10:11] op_sel_hi:[1,0]
	v_pk_fma_f32 v[18:19], v[198:199], v[18:19], v[62:63]
	v_pk_fma_f32 v[20:21], v[192:193], v[20:21], v[64:65]
	global_store_dwordx2 v[148:149], v[12:13], off offset:2048
	v_cvt_pk_bf16_f32 v12, v18, v19
	v_cvt_pk_bf16_f32 v13, v20, v21
	v_pk_mul_f32 v[22:23], v[46:47], v[22:23]
	v_pk_mul_f32 v[24:25], v[48:49], v[24:25]
	global_store_dwordx2 v[146:147], v[12:13], off offset:2048
	ds_write_b128 v173, v[118:121] offset:4096
	ds_write2_b64 v205, v[18:19], v[20:21] offset1:1
	v_cvt_pk_bf16_f32 v12, v122, v123
	v_cvt_pk_bf16_f32 v13, v124, v125
	v_pk_mul_f32 v[88:89], v[110:111], v[10:11] op_sel_hi:[1,0]
	v_pk_mul_f32 v[90:91], v[112:113], v[10:11] op_sel_hi:[1,0]
	v_pk_fma_f32 v[22:23], v[126:127], v[22:23], v[174:175]
	v_pk_fma_f32 v[24:25], v[128:129], v[24:25], v[176:177]
	global_store_dwordx2 v[148:149], v[12:13], off offset:2560
	v_cvt_pk_bf16_f32 v12, v22, v23
	v_cvt_pk_bf16_f32 v13, v24, v25
	v_pk_mul_f32 v[2:3], v[78:79], v[2:3]
	v_pk_mul_f32 v[4:5], v[80:81], v[4:5]
	v_pk_mul_f32 v[92:93], v[114:115], v[10:11] op_sel_hi:[1,0]
	v_pk_mul_f32 v[10:11], v[116:117], v[10:11] op_sel_hi:[1,0]
	v_pk_mul_f32 v[36:37], v[82:83], v[88:89]
	v_pk_mul_f32 v[38:39], v[84:85], v[90:91]
	global_store_dwordx2 v[146:147], v[12:13], off offset:2560
	ds_write_b128 v173, v[122:125] offset:5120
	ds_write2_b64 v206, v[22:23], v[24:25] offset1:1
	v_cvt_pk_bf16_f32 v12, v6, v7
	v_cvt_pk_bf16_f32 v13, v8, v9
	s_waitcnt vmcnt(12)
	v_pk_fma_f32 v[2:3], v[200:201], v[2:3], v[178:179]
	v_pk_fma_f32 v[4:5], v[202:203], v[4:5], v[180:181]
	v_pk_fma_f32 v[36:37], v[138:139], v[36:37], v[182:183]
	v_pk_fma_f32 v[38:39], v[140:141], v[38:39], v[184:185]
	v_pk_mul_f32 v[40:41], v[78:79], v[92:93]
	v_pk_mul_f32 v[10:11], v[80:81], v[10:11]
	global_store_dwordx2 v[148:149], v[12:13], off offset:3072
	v_cvt_pk_bf16_f32 v12, v36, v37
	v_cvt_pk_bf16_f32 v13, v38, v39
	global_store_dwordx2 v[146:147], v[12:13], off offset:3072
	ds_write_b128 v173, v[6:9] offset:6144
	ds_write2_b64 v207, v[36:37], v[38:39] offset1:1
	v_cvt_pk_bf16_f32 v6, v2, v3
	v_cvt_pk_bf16_f32 v7, v4, v5
	v_pk_fma_f32 v[40:41], v[200:201], v[40:41], v[178:179]
	v_pk_fma_f32 v[10:11], v[202:203], v[10:11], v[180:181]
	global_store_dwordx2 v[148:149], v[6:7], off offset:3584
	v_cvt_pk_bf16_f32 v6, v40, v41
	v_cvt_pk_bf16_f32 v7, v10, v11
	global_store_dwordx2 v[146:147], v[6:7], off offset:3584
	ds_write_b128 v173, v[2:5] offset:7168
	ds_write2_b64 v191, v[40:41], v[10:11] offset1:1
	v_and_b32_e32 v20, 15, v1
	s_movk_i32 s0, 0x2008
	v_bfe_u32 v4, v1, 4, 2
	v_mad_u32_u24 v2, v20, s0, 0
	v_lshlrev_b32_e32 v3, 10, v172
	v_lshlrev_b32_e32 v5, 2, v4
	v_add3_u32 v21, v2, v3, v5
	v_lshl_or_b32 v2, v172, 8, v4
	v_ashrrev_i32_e32 v3, 31, v2
	v_lshlrev_b64 v[2:3], 8, v[2:3]
	v_lshl_or_b32 v2, v20, 2, v2
	v_lshl_add_u64 v[18:19], s[8:9], 0, v[2:3]
	s_mov_b64 s[0:1], 0
	v_mov_b32_e32 v2, 0
	v_mov_b32_e32 v3, v143
	v_mov_b32_e32 v4, v143
	v_mov_b32_e32 v5, v143
	v_mov_b32_e32 v6, 0
	v_mov_b32_e32 v7, v143
	v_mov_b32_e32 v8, v143
	v_mov_b32_e32 v9, v143
	v_mov_b32_e32 v10, 0
	v_mov_b32_e32 v11, v143
	v_mov_b32_e32 v12, v143
	v_mov_b32_e32 v13, v143
	v_mov_b32_e32 v14, 0
	v_mov_b32_e32 v15, v143
	v_mov_b32_e32 v16, v143
	v_mov_b32_e32 v17, v143
	s_waitcnt lgkmcnt(0)
	s_barrier
